# router phases: software-pipelined pass 2 (next iteration's 12 global loads issued a whole iteration ahead into spare registers)
# baseline (speedup 1.0000x reference)
.LBB0_580:
	s_lshl_b32 s64, s63, 4
	s_add_i32 s48, s64, s60
	v_add_u32_e32 v0, s48, v93
	v_ashrrev_i32_e32 v1, 31, v0
	v_lshlrev_b64 v[0:1], 11, v[0:1]
	v_lshl_add_u64 v[48:49], v[54:55], 0, v[0:1]
	global_load_dwordx4 v[82:85], v[48:49], off
	global_load_dwordx4 v[86:89], v[48:49], off offset:64
	global_load_dwordx4 v[110:113], v[48:49], off offset:128
	global_load_dwordx4 v[114:117], v[48:49], off offset:192
	global_load_dwordx4 v[44:47], v[48:49], off offset:256
	global_load_dwordx4 v[40:43], v[48:49], off offset:320
	global_load_dwordx4 v[36:39], v[48:49], off offset:384
	global_load_dwordx4 v[32:35], v[48:49], off offset:448
	global_load_dwordx4 v[28:31], v[48:49], off offset:512
	global_load_dwordx4 v[24:27], v[48:49], off offset:576
	global_load_dwordx4 v[20:23], v[48:49], off offset:640
	global_load_dwordx4 v[16:19], v[48:49], off offset:704
	global_load_dwordx4 v[12:15], v[48:49], off offset:768
	global_load_dwordx4 v[8:11], v[48:49], off offset:832
	global_load_dwordx4 v[4:7], v[48:49], off offset:896
	global_load_dwordx4 v[0:3], v[48:49], off offset:960
	v_cmp_lt_i32_e32 vcc, v102, v103
	s_mov_b32 s49, 0x800000
	s_min_i32 s48, s48, 0x8000
	s_ashr_i32 s48, s48, 11
	s_cmp_eq_u32 s48, s65
	s_waitcnt vmcnt(15)
	v_and_b32_e32 v51, 0xffff0000, v82
	v_and_b32_e32 v62, 0xffff0000, v83
	v_lshlrev_b32_e32 v50, 16, v82
	v_lshlrev_b32_e32 v52, 16, v83
	v_and_b32_e32 v66, 0xffff0000, v84
	v_mul_f32_e32 v51, v51, v51
	v_mul_f32_e32 v62, v62, v62
	v_lshlrev_b32_e32 v64, 16, v84
	v_and_b32_e32 v70, 0xffff0000, v85
	v_mul_f32_e32 v66, v66, v66
	v_fmac_f32_e32 v51, v50, v50
	v_fmac_f32_e32 v62, v52, v52
	v_lshlrev_b32_e32 v68, 16, v85
	s_waitcnt vmcnt(14)
	v_and_b32_e32 v74, 0xffff0000, v86
	v_mul_f32_e32 v70, v70, v70
	v_fmac_f32_e32 v66, v64, v64
	v_add_f32_e32 v50, v51, v62
	v_lshlrev_b32_e32 v72, 16, v86
	v_and_b32_e32 v83, 0xffff0000, v87
	v_mul_f32_e32 v74, v74, v74
	v_fmac_f32_e32 v70, v68, v68
	v_add_f32_e32 v50, v66, v50
	v_lshlrev_b32_e32 v82, 16, v87
	v_and_b32_e32 v85, 0xffff0000, v88
	v_mul_f32_e32 v83, v83, v83
	v_fmac_f32_e32 v74, v72, v72
	v_add_f32_e32 v50, v70, v50
	v_lshlrev_b32_e32 v84, 16, v88
	v_and_b32_e32 v87, 0xffff0000, v89
	v_mul_f32_e32 v85, v85, v85
	v_fmac_f32_e32 v83, v82, v82
	v_add_f32_e32 v50, v74, v50
	v_lshlrev_b32_e32 v86, 16, v89
	s_waitcnt vmcnt(13)
	v_and_b32_e32 v89, 0xffff0000, v110
	v_mul_f32_e32 v87, v87, v87
	v_fmac_f32_e32 v85, v84, v84
	v_add_f32_e32 v50, v83, v50
	v_lshlrev_b32_e32 v88, 16, v110
	v_and_b32_e32 v91, 0xffff0000, v111
	v_mul_f32_e32 v89, v89, v89
	v_fmac_f32_e32 v87, v86, v86
	v_add_f32_e32 v50, v85, v50
	v_lshlrev_b32_e32 v90, 16, v111
	v_and_b32_e32 v111, 0xffff0000, v112
	v_mul_f32_e32 v91, v91, v91
	v_fmac_f32_e32 v89, v88, v88
	v_add_f32_e32 v50, v87, v50
	v_lshlrev_b32_e32 v110, 16, v112
	v_lshlrev_b32_e32 v112, 16, v113
	v_and_b32_e32 v113, 0xffff0000, v113
	v_mul_f32_e32 v111, v111, v111
	v_fmac_f32_e32 v91, v90, v90
	v_add_f32_e32 v50, v89, v50
	s_waitcnt vmcnt(12)
	v_lshlrev_b32_e32 v118, 16, v114
	v_and_b32_e32 v114, 0xffff0000, v114
	v_mul_f32_e32 v113, v113, v113
	v_fmac_f32_e32 v111, v110, v110
	v_add_f32_e32 v50, v91, v50
	v_lshlrev_b32_e32 v119, 16, v115
	v_and_b32_e32 v115, 0xffff0000, v115
	v_mul_f32_e32 v114, v114, v114
	v_fmac_f32_e32 v113, v112, v112
	v_add_f32_e32 v50, v111, v50
	v_lshlrev_b32_e32 v120, 16, v116
	v_and_b32_e32 v116, 0xffff0000, v116
	v_mul_f32_e32 v115, v115, v115
	v_fmac_f32_e32 v114, v118, v118
	v_add_f32_e32 v50, v113, v50
	v_lshlrev_b32_e32 v121, 16, v117
	v_and_b32_e32 v117, 0xffff0000, v117
	v_mul_f32_e32 v116, v116, v116
	v_fmac_f32_e32 v115, v119, v119
	v_add_f32_e32 v50, v114, v50
	s_waitcnt vmcnt(11)
	v_lshlrev_b32_e32 v122, 16, v44
	v_and_b32_e32 v44, 0xffff0000, v44
	v_mul_f32_e32 v117, v117, v117
	v_fmac_f32_e32 v116, v120, v120
	v_add_f32_e32 v50, v115, v50
	v_mul_f32_e32 v44, v44, v44
	v_fmac_f32_e32 v117, v121, v121
	v_add_f32_e32 v50, v116, v50
	v_add_f32_e32 v50, v117, v50
	v_fmac_f32_e32 v44, v122, v122
	v_add_f32_e32 v44, v44, v50
	v_lshlrev_b32_e32 v50, 16, v45
	v_and_b32_e32 v45, 0xffff0000, v45
	v_mul_f32_e32 v45, v45, v45
	v_fmac_f32_e32 v45, v50, v50
	v_add_f32_e32 v44, v45, v44
	v_lshlrev_b32_e32 v45, 16, v46
	v_and_b32_e32 v46, 0xffff0000, v46
	v_mul_f32_e32 v46, v46, v46
	v_fmac_f32_e32 v46, v45, v45
	v_add_f32_e32 v44, v46, v44
	v_and_b32_e32 v46, 0xffff0000, v47
	v_lshlrev_b32_e32 v45, 16, v47
	v_mul_f32_e32 v46, v46, v46
	v_fmac_f32_e32 v46, v45, v45
	s_waitcnt vmcnt(10)
	v_lshlrev_b32_e32 v45, 16, v40
	v_and_b32_e32 v40, 0xffff0000, v40
	v_mul_f32_e32 v40, v40, v40
	v_add_f32_e32 v44, v46, v44
	v_fmac_f32_e32 v40, v45, v45
	v_add_f32_e32 v40, v40, v44
	v_lshlrev_b32_e32 v44, 16, v41
	v_and_b32_e32 v41, 0xffff0000, v41
	v_mul_f32_e32 v41, v41, v41
	v_fmac_f32_e32 v41, v44, v44
	v_add_f32_e32 v40, v41, v40
	v_lshlrev_b32_e32 v41, 16, v42
	v_and_b32_e32 v42, 0xffff0000, v42
	v_mul_f32_e32 v42, v42, v42
	v_fmac_f32_e32 v42, v41, v41
	v_add_f32_e32 v40, v42, v40
	v_and_b32_e32 v42, 0xffff0000, v43
	v_lshlrev_b32_e32 v41, 16, v43
	v_mul_f32_e32 v42, v42, v42
	v_fmac_f32_e32 v42, v41, v41
	s_waitcnt vmcnt(9)
	v_lshlrev_b32_e32 v41, 16, v36
	v_and_b32_e32 v36, 0xffff0000, v36
	v_mul_f32_e32 v36, v36, v36
	v_add_f32_e32 v40, v42, v40
	v_fmac_f32_e32 v36, v41, v41
	v_add_f32_e32 v36, v36, v40
	v_lshlrev_b32_e32 v40, 16, v37
	v_and_b32_e32 v37, 0xffff0000, v37
	v_mul_f32_e32 v37, v37, v37
	v_fmac_f32_e32 v37, v40, v40
	v_add_f32_e32 v36, v37, v36
	v_lshlrev_b32_e32 v37, 16, v38
	v_and_b32_e32 v38, 0xffff0000, v38
	v_mul_f32_e32 v38, v38, v38
	v_fmac_f32_e32 v38, v37, v37
	v_add_f32_e32 v36, v38, v36
	v_and_b32_e32 v38, 0xffff0000, v39
	v_lshlrev_b32_e32 v37, 16, v39
	v_mul_f32_e32 v38, v38, v38
	v_fmac_f32_e32 v38, v37, v37
	s_waitcnt vmcnt(8)
	v_lshlrev_b32_e32 v37, 16, v32
	v_and_b32_e32 v32, 0xffff0000, v32
	v_mul_f32_e32 v32, v32, v32
	v_add_f32_e32 v36, v38, v36
	v_fmac_f32_e32 v32, v37, v37
	v_add_f32_e32 v32, v32, v36
	v_lshlrev_b32_e32 v36, 16, v33
	v_and_b32_e32 v33, 0xffff0000, v33
	v_mul_f32_e32 v33, v33, v33
	v_fmac_f32_e32 v33, v36, v36
	v_add_f32_e32 v32, v33, v32
	v_lshlrev_b32_e32 v33, 16, v34
	v_and_b32_e32 v34, 0xffff0000, v34
	v_mul_f32_e32 v34, v34, v34
	v_fmac_f32_e32 v34, v33, v33
	v_add_f32_e32 v32, v34, v32
	v_and_b32_e32 v34, 0xffff0000, v35
	v_lshlrev_b32_e32 v33, 16, v35
	v_mul_f32_e32 v34, v34, v34
	v_fmac_f32_e32 v34, v33, v33
	s_waitcnt vmcnt(7)
	v_lshlrev_b32_e32 v33, 16, v28
	v_and_b32_e32 v28, 0xffff0000, v28
	v_mul_f32_e32 v28, v28, v28
	v_add_f32_e32 v32, v34, v32
	v_fmac_f32_e32 v28, v33, v33
	v_add_f32_e32 v28, v28, v32
	v_lshlrev_b32_e32 v32, 16, v29
	v_and_b32_e32 v29, 0xffff0000, v29
	v_mul_f32_e32 v29, v29, v29
	v_fmac_f32_e32 v29, v32, v32
	v_add_f32_e32 v28, v29, v28
	v_lshlrev_b32_e32 v29, 16, v30
	v_and_b32_e32 v30, 0xffff0000, v30
	v_mul_f32_e32 v30, v30, v30
	v_fmac_f32_e32 v30, v29, v29
	v_add_f32_e32 v28, v30, v28
	v_and_b32_e32 v30, 0xffff0000, v31
	v_lshlrev_b32_e32 v29, 16, v31
	v_mul_f32_e32 v30, v30, v30
	v_fmac_f32_e32 v30, v29, v29
	s_waitcnt vmcnt(6)
	v_lshlrev_b32_e32 v29, 16, v24
	v_and_b32_e32 v24, 0xffff0000, v24
	v_mul_f32_e32 v24, v24, v24
	v_add_f32_e32 v28, v30, v28
	v_fmac_f32_e32 v24, v29, v29
	v_add_f32_e32 v24, v24, v28
	v_lshlrev_b32_e32 v28, 16, v25
	v_and_b32_e32 v25, 0xffff0000, v25
	v_mul_f32_e32 v25, v25, v25
	v_fmac_f32_e32 v25, v28, v28
	v_add_f32_e32 v24, v25, v24
	v_lshlrev_b32_e32 v25, 16, v26
	v_and_b32_e32 v26, 0xffff0000, v26
	v_mul_f32_e32 v26, v26, v26
	v_fmac_f32_e32 v26, v25, v25
	v_add_f32_e32 v24, v26, v24
	v_and_b32_e32 v26, 0xffff0000, v27
	v_lshlrev_b32_e32 v25, 16, v27
	v_mul_f32_e32 v26, v26, v26
	v_fmac_f32_e32 v26, v25, v25
	s_waitcnt vmcnt(5)
	v_lshlrev_b32_e32 v25, 16, v20
	v_and_b32_e32 v20, 0xffff0000, v20
	v_mul_f32_e32 v20, v20, v20
	v_add_f32_e32 v24, v26, v24
	v_fmac_f32_e32 v20, v25, v25
	v_add_f32_e32 v20, v20, v24
	v_lshlrev_b32_e32 v24, 16, v21
	v_and_b32_e32 v21, 0xffff0000, v21
	v_mul_f32_e32 v21, v21, v21
	v_fmac_f32_e32 v21, v24, v24
	v_add_f32_e32 v20, v21, v20
	v_lshlrev_b32_e32 v21, 16, v22
	v_and_b32_e32 v22, 0xffff0000, v22
	v_mul_f32_e32 v22, v22, v22
	v_fmac_f32_e32 v22, v21, v21
	v_add_f32_e32 v20, v22, v20
	v_and_b32_e32 v22, 0xffff0000, v23
	v_lshlrev_b32_e32 v21, 16, v23
	v_mul_f32_e32 v22, v22, v22
	v_fmac_f32_e32 v22, v21, v21
	s_waitcnt vmcnt(4)
	v_lshlrev_b32_e32 v21, 16, v16
	v_and_b32_e32 v16, 0xffff0000, v16
	v_mul_f32_e32 v16, v16, v16
	v_add_f32_e32 v20, v22, v20
	v_fmac_f32_e32 v16, v21, v21
	v_add_f32_e32 v16, v16, v20
	v_lshlrev_b32_e32 v20, 16, v17
	v_and_b32_e32 v17, 0xffff0000, v17
	v_mul_f32_e32 v17, v17, v17
	v_fmac_f32_e32 v17, v20, v20
	v_add_f32_e32 v16, v17, v16
	v_lshlrev_b32_e32 v17, 16, v18
	v_and_b32_e32 v18, 0xffff0000, v18
	v_mul_f32_e32 v18, v18, v18
	v_fmac_f32_e32 v18, v17, v17
	v_add_f32_e32 v16, v18, v16
	v_and_b32_e32 v18, 0xffff0000, v19
	v_lshlrev_b32_e32 v17, 16, v19
	v_mul_f32_e32 v18, v18, v18
	v_fmac_f32_e32 v18, v17, v17
	s_waitcnt vmcnt(3)
	v_lshlrev_b32_e32 v17, 16, v12
	v_and_b32_e32 v12, 0xffff0000, v12
	v_mul_f32_e32 v12, v12, v12
	v_add_f32_e32 v16, v18, v16
	v_fmac_f32_e32 v12, v17, v17
	v_add_f32_e32 v12, v12, v16
	v_lshlrev_b32_e32 v16, 16, v13
	v_and_b32_e32 v13, 0xffff0000, v13
	v_mul_f32_e32 v13, v13, v13
	v_fmac_f32_e32 v13, v16, v16
	global_load_dwordx4 v[16:19], v[48:49], off offset:1024
	global_load_dwordx4 v[28:31], v[48:49], off offset:1088
	v_add_f32_e32 v12, v13, v12
	v_lshlrev_b32_e32 v13, 16, v14
	v_and_b32_e32 v14, 0xffff0000, v14
	v_mul_f32_e32 v14, v14, v14
	v_fmac_f32_e32 v14, v13, v13
	v_add_f32_e32 v12, v14, v12
	v_and_b32_e32 v14, 0xffff0000, v15
	v_lshlrev_b32_e32 v13, 16, v15
	v_mul_f32_e32 v14, v14, v14
	global_load_dwordx4 v[32:35], v[48:49], off offset:1152
	global_load_dwordx4 v[36:39], v[48:49], off offset:1216
	v_fmac_f32_e32 v14, v13, v13
	s_waitcnt vmcnt(6)
	v_lshlrev_b32_e32 v13, 16, v8
	v_and_b32_e32 v8, 0xffff0000, v8
	v_mul_f32_e32 v8, v8, v8
	v_add_f32_e32 v12, v14, v12
	v_fmac_f32_e32 v8, v13, v13
	v_add_f32_e32 v8, v8, v12
	v_lshlrev_b32_e32 v12, 16, v9
	v_and_b32_e32 v9, 0xffff0000, v9
	v_mul_f32_e32 v9, v9, v9
	v_fmac_f32_e32 v9, v12, v12
	v_add_f32_e32 v8, v9, v8
	v_lshlrev_b32_e32 v9, 16, v10
	v_and_b32_e32 v10, 0xffff0000, v10
	v_mul_f32_e32 v10, v10, v10
	v_fmac_f32_e32 v10, v9, v9
	v_add_f32_e32 v8, v10, v8
	v_and_b32_e32 v10, 0xffff0000, v11
	v_lshlrev_b32_e32 v9, 16, v11
	v_mul_f32_e32 v10, v10, v10
	v_fmac_f32_e32 v10, v9, v9
	s_waitcnt vmcnt(5)
	v_lshlrev_b32_e32 v9, 16, v4
	v_and_b32_e32 v4, 0xffff0000, v4
	v_mul_f32_e32 v4, v4, v4
	v_add_f32_e32 v8, v10, v8
	v_fmac_f32_e32 v4, v9, v9
	v_add_f32_e32 v4, v4, v8
	v_lshlrev_b32_e32 v8, 16, v5
	v_and_b32_e32 v5, 0xffff0000, v5
	v_mul_f32_e32 v5, v5, v5
	v_fmac_f32_e32 v5, v8, v8
	v_add_f32_e32 v4, v5, v4
	v_lshlrev_b32_e32 v5, 16, v6
	v_and_b32_e32 v6, 0xffff0000, v6
	v_mul_f32_e32 v6, v6, v6
	v_fmac_f32_e32 v6, v5, v5
	v_add_f32_e32 v4, v6, v4
	v_and_b32_e32 v6, 0xffff0000, v7
	v_lshlrev_b32_e32 v5, 16, v7
	v_mul_f32_e32 v6, v6, v6
	v_fmac_f32_e32 v6, v5, v5
	s_waitcnt vmcnt(4)
	v_lshlrev_b32_e32 v5, 16, v0
	v_and_b32_e32 v0, 0xffff0000, v0
	v_mul_f32_e32 v0, v0, v0
	v_add_f32_e32 v4, v6, v4
	v_fmac_f32_e32 v0, v5, v5
	v_add_f32_e32 v0, v0, v4
	v_lshlrev_b32_e32 v4, 16, v1
	v_and_b32_e32 v1, 0xffff0000, v1
	v_mul_f32_e32 v1, v1, v1
	v_fmac_f32_e32 v1, v4, v4
	v_add_f32_e32 v0, v1, v0
	v_lshlrev_b32_e32 v1, 16, v2
	v_and_b32_e32 v2, 0xffff0000, v2
	v_mul_f32_e32 v2, v2, v2
	v_fmac_f32_e32 v2, v1, v1
	v_add_f32_e32 v0, v2, v0
	v_and_b32_e32 v2, 0xffff0000, v3
	v_lshlrev_b32_e32 v1, 16, v3
	v_mul_f32_e32 v2, v2, v2
	v_fmac_f32_e32 v2, v1, v1
	v_add_f32_e32 v50, v2, v0
	global_load_dwordx4 v[40:43], v[48:49], off offset:1280
	global_load_dwordx4 v[44:47], v[48:49], off offset:1344
	global_load_dwordx4 v[82:85], v[48:49], off offset:1408
	global_load_dwordx4 v[86:89], v[48:49], off offset:1472
	global_load_dwordx4 v[110:113], v[48:49], off offset:1536
	global_load_dwordx4 v[114:117], v[48:49], off offset:1600
	global_load_dwordx4 v[24:27], v[48:49], off offset:1664
	global_load_dwordx4 v[20:23], v[48:49], off offset:1728
	global_load_dwordx4 v[12:15], v[48:49], off offset:1792
	global_load_dwordx4 v[8:11], v[48:49], off offset:1856
	global_load_dwordx4 v[4:7], v[48:49], off offset:1920
	global_load_dwordx4 v[0:3], v[48:49], off offset:1984
	v_mov_b32_e32 v62, v99
	v_mov_b32_e32 v64, v98
	v_mov_b32_e32 v66, v97
	s_waitcnt vmcnt(15)
	v_lshlrev_b32_e32 v48, 16, v16
	v_and_b32_e32 v16, 0xffff0000, v16
	v_mul_f32_e32 v16, v16, v16
	v_fmac_f32_e32 v16, v48, v48
	v_lshlrev_b32_e32 v48, 16, v17
	v_and_b32_e32 v17, 0xffff0000, v17
	v_mul_f32_e32 v17, v17, v17
	v_add_f32_e32 v16, v16, v50
	v_fmac_f32_e32 v17, v48, v48
	v_add_f32_e32 v16, v17, v16
	v_lshlrev_b32_e32 v17, 16, v18
	v_and_b32_e32 v18, 0xffff0000, v18
	v_mul_f32_e32 v18, v18, v18
	v_fmac_f32_e32 v18, v17, v17
	v_add_f32_e32 v16, v18, v16
	v_and_b32_e32 v18, 0xffff0000, v19
	v_lshlrev_b32_e32 v17, 16, v19
	v_mul_f32_e32 v18, v18, v18
	v_fmac_f32_e32 v18, v17, v17
	v_add_f32_e32 v16, v18, v16
	s_waitcnt vmcnt(14)
	v_and_b32_e32 v18, 0xffff0000, v28
	v_lshlrev_b32_e32 v17, 16, v28
	v_mul_f32_e32 v18, v18, v18
	v_fmac_f32_e32 v18, v17, v17
	v_add_f32_e32 v16, v18, v16
	v_and_b32_e32 v18, 0xffff0000, v29
	v_lshlrev_b32_e32 v17, 16, v29
	v_mul_f32_e32 v18, v18, v18
	v_fmac_f32_e32 v18, v17, v17
	v_add_f32_e32 v16, v18, v16
	v_and_b32_e32 v18, 0xffff0000, v30
	v_lshlrev_b32_e32 v17, 16, v30
	v_mul_f32_e32 v18, v18, v18
	v_fmac_f32_e32 v18, v17, v17
	v_add_f32_e32 v16, v18, v16
	v_and_b32_e32 v18, 0xffff0000, v31
	v_lshlrev_b32_e32 v17, 16, v31
	v_mul_f32_e32 v18, v18, v18
	v_fmac_f32_e32 v18, v17, v17
	v_add_f32_e32 v16, v18, v16
	s_waitcnt vmcnt(13)
	v_and_b32_e32 v18, 0xffff0000, v32
	v_lshlrev_b32_e32 v17, 16, v32
	v_mul_f32_e32 v18, v18, v18
	v_fmac_f32_e32 v18, v17, v17
	v_add_f32_e32 v16, v18, v16
	v_and_b32_e32 v18, 0xffff0000, v33
	v_lshlrev_b32_e32 v17, 16, v33
	v_mul_f32_e32 v18, v18, v18
	v_fmac_f32_e32 v18, v17, v17
	v_add_f32_e32 v16, v18, v16
	v_and_b32_e32 v18, 0xffff0000, v34
	v_lshlrev_b32_e32 v17, 16, v34
	v_mul_f32_e32 v18, v18, v18
	v_fmac_f32_e32 v18, v17, v17
	v_add_f32_e32 v16, v18, v16
	v_and_b32_e32 v18, 0xffff0000, v35
	v_lshlrev_b32_e32 v17, 16, v35
	v_mul_f32_e32 v18, v18, v18
	v_fmac_f32_e32 v18, v17, v17
	v_add_f32_e32 v16, v18, v16
	s_waitcnt vmcnt(12)
	v_and_b32_e32 v18, 0xffff0000, v36
	v_lshlrev_b32_e32 v17, 16, v36
	v_mul_f32_e32 v18, v18, v18
	v_fmac_f32_e32 v18, v17, v17
	v_add_f32_e32 v16, v18, v16
	v_and_b32_e32 v18, 0xffff0000, v37
	v_lshlrev_b32_e32 v17, 16, v37
	v_mul_f32_e32 v18, v18, v18
	v_fmac_f32_e32 v18, v17, v17
	v_add_f32_e32 v16, v18, v16
	v_and_b32_e32 v18, 0xffff0000, v38
	v_lshlrev_b32_e32 v17, 16, v38
	v_mul_f32_e32 v18, v18, v18
	v_fmac_f32_e32 v18, v17, v17
	v_add_f32_e32 v16, v18, v16
	v_and_b32_e32 v18, 0xffff0000, v39
	v_lshlrev_b32_e32 v17, 16, v39
	v_mul_f32_e32 v18, v18, v18
	v_fmac_f32_e32 v18, v17, v17
	v_add_f32_e32 v16, v18, v16
	s_waitcnt vmcnt(11)
	v_and_b32_e32 v18, 0xffff0000, v40
	v_lshlrev_b32_e32 v17, 16, v40
	v_mul_f32_e32 v18, v18, v18
	v_fmac_f32_e32 v18, v17, v17
	v_add_f32_e32 v16, v18, v16
	v_and_b32_e32 v18, 0xffff0000, v41
	v_lshlrev_b32_e32 v17, 16, v41
	v_mul_f32_e32 v18, v18, v18
	v_fmac_f32_e32 v18, v17, v17
	v_add_f32_e32 v16, v18, v16
	v_and_b32_e32 v18, 0xffff0000, v42
	v_lshlrev_b32_e32 v17, 16, v42
	v_mul_f32_e32 v18, v18, v18
	v_fmac_f32_e32 v18, v17, v17
	v_add_f32_e32 v16, v18, v16
	v_and_b32_e32 v18, 0xffff0000, v43
	v_lshlrev_b32_e32 v17, 16, v43
	v_mul_f32_e32 v18, v18, v18
	v_fmac_f32_e32 v18, v17, v17
	v_add_f32_e32 v16, v18, v16
	s_waitcnt vmcnt(10)
	v_and_b32_e32 v18, 0xffff0000, v44
	v_lshlrev_b32_e32 v17, 16, v44
	v_mul_f32_e32 v18, v18, v18
	v_fmac_f32_e32 v18, v17, v17
	v_add_f32_e32 v16, v18, v16
	v_and_b32_e32 v18, 0xffff0000, v45
	v_lshlrev_b32_e32 v17, 16, v45
	v_mul_f32_e32 v18, v18, v18
	v_fmac_f32_e32 v18, v17, v17
	v_add_f32_e32 v16, v18, v16
	v_and_b32_e32 v18, 0xffff0000, v46
	v_lshlrev_b32_e32 v17, 16, v46
	v_mul_f32_e32 v18, v18, v18
	v_fmac_f32_e32 v18, v17, v17
	v_add_f32_e32 v16, v18, v16
	v_and_b32_e32 v18, 0xffff0000, v47
	v_lshlrev_b32_e32 v17, 16, v47
	v_mul_f32_e32 v18, v18, v18
	v_fmac_f32_e32 v18, v17, v17
	v_add_f32_e32 v16, v18, v16
	s_waitcnt vmcnt(9)
	v_and_b32_e32 v18, 0xffff0000, v82
	v_lshlrev_b32_e32 v17, 16, v82
	v_mul_f32_e32 v18, v18, v18
	v_fmac_f32_e32 v18, v17, v17
	v_add_f32_e32 v16, v18, v16
	v_and_b32_e32 v18, 0xffff0000, v83
	v_lshlrev_b32_e32 v17, 16, v83
	v_mul_f32_e32 v18, v18, v18
	v_fmac_f32_e32 v18, v17, v17
	v_add_f32_e32 v16, v18, v16
	v_and_b32_e32 v18, 0xffff0000, v84
	v_lshlrev_b32_e32 v17, 16, v84
	v_mul_f32_e32 v18, v18, v18
	v_fmac_f32_e32 v18, v17, v17
	v_add_f32_e32 v16, v18, v16
	v_and_b32_e32 v18, 0xffff0000, v85
	v_lshlrev_b32_e32 v17, 16, v85
	v_mul_f32_e32 v18, v18, v18
	v_fmac_f32_e32 v18, v17, v17
	v_add_f32_e32 v16, v18, v16
	s_waitcnt vmcnt(8)
	v_and_b32_e32 v18, 0xffff0000, v86
	v_lshlrev_b32_e32 v17, 16, v86
	v_mul_f32_e32 v18, v18, v18
	v_fmac_f32_e32 v18, v17, v17
	v_add_f32_e32 v16, v18, v16
	v_and_b32_e32 v18, 0xffff0000, v87
	v_lshlrev_b32_e32 v17, 16, v87
	v_mul_f32_e32 v18, v18, v18
	v_fmac_f32_e32 v18, v17, v17
	v_add_f32_e32 v16, v18, v16
	v_and_b32_e32 v18, 0xffff0000, v88
	v_lshlrev_b32_e32 v17, 16, v88
	v_mul_f32_e32 v18, v18, v18
	v_fmac_f32_e32 v18, v17, v17
	v_add_f32_e32 v16, v18, v16
	v_and_b32_e32 v18, 0xffff0000, v89
	v_lshlrev_b32_e32 v17, 16, v89
	v_mul_f32_e32 v18, v18, v18
	v_fmac_f32_e32 v18, v17, v17
	v_add_f32_e32 v16, v18, v16
	s_waitcnt vmcnt(7)
	v_and_b32_e32 v18, 0xffff0000, v110
	v_lshlrev_b32_e32 v17, 16, v110
	v_mul_f32_e32 v18, v18, v18
	v_fmac_f32_e32 v18, v17, v17
	v_add_f32_e32 v16, v18, v16
	v_and_b32_e32 v18, 0xffff0000, v111
	v_lshlrev_b32_e32 v17, 16, v111
	v_mul_f32_e32 v18, v18, v18
	v_fmac_f32_e32 v18, v17, v17
	v_add_f32_e32 v16, v18, v16
	v_and_b32_e32 v18, 0xffff0000, v112
	v_lshlrev_b32_e32 v17, 16, v112
	v_mul_f32_e32 v18, v18, v18
	v_fmac_f32_e32 v18, v17, v17
	v_add_f32_e32 v16, v18, v16
	v_and_b32_e32 v18, 0xffff0000, v113
	v_lshlrev_b32_e32 v17, 16, v113
	v_mul_f32_e32 v18, v18, v18
	v_fmac_f32_e32 v18, v17, v17
	v_add_f32_e32 v16, v18, v16
	s_waitcnt vmcnt(6)
	v_and_b32_e32 v18, 0xffff0000, v114
	v_lshlrev_b32_e32 v17, 16, v114
	v_mul_f32_e32 v18, v18, v18
	v_fmac_f32_e32 v18, v17, v17
	v_add_f32_e32 v16, v18, v16
	v_and_b32_e32 v18, 0xffff0000, v115
	v_lshlrev_b32_e32 v17, 16, v115
	v_mul_f32_e32 v18, v18, v18
	v_fmac_f32_e32 v18, v17, v17
	v_add_f32_e32 v16, v18, v16
	v_and_b32_e32 v18, 0xffff0000, v116
	v_lshlrev_b32_e32 v17, 16, v116
	v_mul_f32_e32 v18, v18, v18
	v_fmac_f32_e32 v18, v17, v17
	v_add_f32_e32 v16, v18, v16
	v_and_b32_e32 v18, 0xffff0000, v117
	v_lshlrev_b32_e32 v17, 16, v117
	v_mul_f32_e32 v18, v18, v18
	v_fmac_f32_e32 v18, v17, v17
	v_add_f32_e32 v16, v18, v16
	s_waitcnt vmcnt(5)
	v_and_b32_e32 v18, 0xffff0000, v24
	v_lshlrev_b32_e32 v17, 16, v24
	v_mul_f32_e32 v18, v18, v18
	v_fmac_f32_e32 v18, v17, v17
	v_add_f32_e32 v16, v18, v16
	v_and_b32_e32 v18, 0xffff0000, v25
	v_lshlrev_b32_e32 v17, 16, v25
	v_mul_f32_e32 v18, v18, v18
	v_fmac_f32_e32 v18, v17, v17
	v_add_f32_e32 v16, v18, v16
	v_and_b32_e32 v18, 0xffff0000, v26
	v_lshlrev_b32_e32 v17, 16, v26
	v_mul_f32_e32 v18, v18, v18
	v_fmac_f32_e32 v18, v17, v17
	v_add_f32_e32 v16, v18, v16
	v_and_b32_e32 v18, 0xffff0000, v27
	v_lshlrev_b32_e32 v17, 16, v27
	v_mul_f32_e32 v18, v18, v18
	v_fmac_f32_e32 v18, v17, v17
	v_add_f32_e32 v16, v18, v16
	s_waitcnt vmcnt(4)
	v_and_b32_e32 v18, 0xffff0000, v20
	v_lshlrev_b32_e32 v17, 16, v20
	v_mul_f32_e32 v18, v18, v18
	v_fmac_f32_e32 v18, v17, v17
	v_add_f32_e32 v16, v18, v16
	v_and_b32_e32 v18, 0xffff0000, v21
	v_lshlrev_b32_e32 v17, 16, v21
	v_mul_f32_e32 v18, v18, v18
	v_fmac_f32_e32 v18, v17, v17
	v_add_f32_e32 v16, v18, v16
	v_and_b32_e32 v18, 0xffff0000, v22
	v_lshlrev_b32_e32 v17, 16, v22
	v_mul_f32_e32 v18, v18, v18
	v_fmac_f32_e32 v18, v17, v17
	v_add_f32_e32 v16, v18, v16
	v_and_b32_e32 v18, 0xffff0000, v23
	v_lshlrev_b32_e32 v17, 16, v23
	v_mul_f32_e32 v18, v18, v18
	v_fmac_f32_e32 v18, v17, v17
	s_waitcnt vmcnt(3)
	v_lshlrev_b32_e32 v17, 16, v12
	v_and_b32_e32 v12, 0xffff0000, v12
	v_mul_f32_e32 v12, v12, v12
	v_add_f32_e32 v16, v18, v16
	v_fmac_f32_e32 v12, v17, v17
	v_add_f32_e32 v12, v12, v16
	v_lshlrev_b32_e32 v16, 16, v13
	v_and_b32_e32 v13, 0xffff0000, v13
	v_mul_f32_e32 v13, v13, v13
	v_fmac_f32_e32 v13, v16, v16
	v_add_f32_e32 v12, v13, v12
	v_lshlrev_b32_e32 v13, 16, v14
	v_and_b32_e32 v14, 0xffff0000, v14
	v_mul_f32_e32 v14, v14, v14
	v_fmac_f32_e32 v14, v13, v13
	v_add_f32_e32 v12, v14, v12
	v_and_b32_e32 v14, 0xffff0000, v15
	v_lshlrev_b32_e32 v13, 16, v15
	v_mul_f32_e32 v14, v14, v14
	v_fmac_f32_e32 v14, v13, v13
	s_waitcnt vmcnt(2)
	v_lshlrev_b32_e32 v13, 16, v8
	v_and_b32_e32 v8, 0xffff0000, v8
	v_mul_f32_e32 v8, v8, v8
	v_add_f32_e32 v12, v14, v12
	v_fmac_f32_e32 v8, v13, v13
	v_add_f32_e32 v8, v8, v12
	v_lshlrev_b32_e32 v12, 16, v9
	v_and_b32_e32 v9, 0xffff0000, v9
	v_mul_f32_e32 v9, v9, v9
	v_fmac_f32_e32 v9, v12, v12
	v_add_f32_e32 v8, v9, v8
	v_lshlrev_b32_e32 v9, 16, v10
	v_and_b32_e32 v10, 0xffff0000, v10
	v_mul_f32_e32 v10, v10, v10
	v_fmac_f32_e32 v10, v9, v9
	v_add_f32_e32 v8, v10, v8
	v_and_b32_e32 v10, 0xffff0000, v11
	v_lshlrev_b32_e32 v9, 16, v11
	v_mul_f32_e32 v10, v10, v10
	v_fmac_f32_e32 v10, v9, v9
	v_add_f32_e32 v10, v10, v8
	s_waitcnt vmcnt(1)
	v_lshlrev_b32_e32 v9, 16, v5
	v_lshlrev_b32_e32 v8, 16, v4
	v_and_b32_e32 v5, 0xffff0000, v5
	v_and_b32_e32 v4, 0xffff0000, v4
	v_pk_mul_f32 v[4:5], v[4:5], v[4:5]
	v_mov_b64_e32 v[86:87], v[80:81]
	v_pk_fma_f32 v[4:5], v[8:9], v[8:9], v[4:5]
	v_mov_b64_e32 v[88:89], v[76:77]
	v_add_f32_e32 v4, v4, v10
	v_add_f32_e32 v8, v5, v4
	v_lshlrev_b32_e32 v5, 16, v7
	v_lshlrev_b32_e32 v4, 16, v6
	v_and_b32_e32 v7, 0xffff0000, v7
	v_and_b32_e32 v6, 0xffff0000, v6
	v_pk_mul_f32 v[6:7], v[6:7], v[6:7]
	v_mov_b32_e32 v68, v96
	v_pk_fma_f32 v[4:5], v[4:5], v[4:5], v[6:7]
	v_mov_b32_e32 v7, v59
	v_add_f32_e32 v4, v4, v8
	v_add_f32_e32 v6, v5, v4
	s_waitcnt vmcnt(0)
	v_lshlrev_b32_e32 v5, 16, v1
	v_lshlrev_b32_e32 v4, 16, v0
	v_and_b32_e32 v1, 0xffff0000, v1
	v_and_b32_e32 v0, 0xffff0000, v0
	v_pk_mul_f32 v[0:1], v[0:1], v[0:1]
	s_nop 0
	v_pk_fma_f32 v[0:1], v[4:5], v[4:5], v[0:1]
	v_mov_b32_e32 v5, v59
	v_add_f32_e32 v0, v0, v6
	v_add_f32_e32 v4, v1, v0
	v_lshlrev_b32_e32 v1, 16, v3
	v_lshlrev_b32_e32 v0, 16, v2
	v_and_b32_e32 v3, 0xffff0000, v3
	v_and_b32_e32 v2, 0xffff0000, v2
	v_pk_mul_f32 v[2:3], v[2:3], v[2:3]
	v_mov_b32_e32 v6, v59
	v_pk_fma_f32 v[0:1], v[0:1], v[0:1], v[2:3]
	v_mov_b32_e32 v2, v59
	v_add_f32_e32 v0, v0, v4
	v_add_f32_e32 v0, v1, v0
	v_cndmask_b32_e32 v1, v101, v102, vcc
	v_lshlrev_b32_e32 v1, 2, v1
	ds_bpermute_b32 v1, v1, v0
	v_cmp_lt_i32_e32 vcc, v104, v103
	v_mov_b32_e32 v4, 0
	v_mov_b32_e32 v3, v59
	s_waitcnt lgkmcnt(0)
	v_add_f32_e32 v0, v0, v1
	v_cndmask_b32_e32 v1, v101, v104, vcc
	v_lshlrev_b32_e32 v1, 2, v1
	ds_bpermute_b32 v1, v1, v0
	s_waitcnt lgkmcnt(0)
	v_add_f32_e32 v0, v0, v1
	v_fmamk_f32 v0, v0, 0x3a800000, v105
	v_mul_f32_e32 v1, 0x4b800000, v0
	v_cmp_gt_f32_e32 vcc, s49, v0
	s_cselect_b32 s49, 0, 0x1000
	v_add_u32_e32 v52, s49, v100
	v_cndmask_b32_e32 v0, v0, v1, vcc
	v_rsq_f32_e32 v0, v0
	v_mad_i64_i32 v[84:85], s[48:49], s48, v106, v[78:79]
	s_mov_b32 s48, 8
	v_mul_f32_e32 v1, 0x45800000, v0
	v_cndmask_b32_e32 v82, v0, v1, vcc
	v_mov_b32_e32 v83, v82
	v_mov_b32_e32 v0, 0
	v_mov_b32_e32 v1, v59
	v_lshl_add_u64 v[176:177], s[52:53], 0, v[88:89]
	global_load_dwordx4 v[128:131], v[176:177], off offset:-128
	v_lshl_add_u64 v[180:181], s[52:53], 0, v[84:85]
	s_mov_b32 s49, 0x103000
	v_add_co_u32_e32 v182, vcc, s49, v180
	s_mov_b64 s[50:51], 0x103000
	s_nop 0
	v_addc_co_u32_e32 v183, vcc, 0, v181, vcc
	v_lshl_add_u64 v[178:179], v[180:181], 0, s[50:51]
	global_load_dwordx4 v[132:135], v[182:183], off
	global_load_dwordx4 v[136:139], v[178:179], off offset:16
	global_load_dwordx4 v[140:143], v[176:177], off offset:-64
	s_mov_b64 s[50:51], 0x103080
	v_lshl_add_u64 v[178:179], v[180:181], 0, s[50:51]
	global_load_dwordx4 v[144:147], v[182:183], off offset:128
	global_load_dwordx4 v[148:151], v[178:179], off offset:16
	global_load_dwordx4 v[152:155], v[176:177], off
	s_mov_b64 s[50:51], 0x103100
	v_lshl_add_u64 v[178:179], v[180:181], 0, s[50:51]
	s_mov_b64 s[50:51], 0x103180
	v_lshl_add_u64 v[180:181], v[180:181], 0, s[50:51]
	global_load_dwordx4 v[156:159], v[182:183], off offset:256
	global_load_dwordx4 v[160:163], v[178:179], off offset:16
	global_load_dwordx4 v[164:167], v[176:177], off offset:64
	global_load_dwordx4 v[168:171], v[182:183], off offset:384
	global_load_dwordx4 v[172:175], v[180:181], off offset:16
.LBB0_581:
	s_waitcnt vmcnt(0)
	v_mov_b64_e32 v[44:45], v[128:129]
	v_mov_b64_e32 v[46:47], v[130:131]
	v_mov_b64_e32 v[48:49], v[132:133]
	v_mov_b64_e32 v[50:51], v[134:135]
	v_mov_b64_e32 v[110:111], v[136:137]
	v_mov_b64_e32 v[112:113], v[138:139]
	v_mov_b64_e32 v[32:33], v[140:141]
	v_mov_b64_e32 v[34:35], v[142:143]
	v_mov_b64_e32 v[40:41], v[144:145]
	v_mov_b64_e32 v[42:43], v[146:147]
	v_mov_b64_e32 v[36:37], v[148:149]
	v_mov_b64_e32 v[38:39], v[150:151]
	v_mov_b64_e32 v[20:21], v[152:153]
	v_mov_b64_e32 v[22:23], v[154:155]
	v_mov_b64_e32 v[28:29], v[156:157]
	v_mov_b64_e32 v[30:31], v[158:159]
	v_mov_b64_e32 v[24:25], v[160:161]
	v_mov_b64_e32 v[26:27], v[162:163]
	v_mov_b64_e32 v[8:9], v[164:165]
	v_mov_b64_e32 v[10:11], v[166:167]
	v_mov_b64_e32 v[16:17], v[168:169]
	v_mov_b64_e32 v[18:19], v[170:171]
	v_mov_b64_e32 v[12:13], v[172:173]
	v_mov_b64_e32 v[14:15], v[174:175]
	v_add_u32_e32 v70, 0, v52
	v_add_u32_e32 v72, 0x20000, v70
	ds_read_b128 v[114:117], v72
	v_add_u32_e32 v72, 0x20010, v70
	ds_read_b128 v[118:121], v72
	v_add_u32_e32 v72, 0, v62
	v_add_u32_e32 v74, 0x10000, v72
	s_mov_b64 s[50:51], 0x100
	v_lshl_add_u64 v[88:89], v[88:89], 0, s[50:51]
	s_mov_b64 s[50:51], 0x200
	s_add_i32 s48, s48, -1
	v_lshl_add_u64 v[84:85], v[84:85], 0, s[50:51]
	s_mov_b64 s[50:51], 0x80
	v_add_u32_e32 v62, 0x100, v62
	v_add_u32_e32 v52, 0x200, v52
	s_cmp_eq_u32 s48, 0
	s_cbranch_scc1 .Lrtpf_skip_a
	v_lshl_add_u64 v[176:177], s[52:53], 0, v[88:89]
	global_load_dwordx4 v[128:131], v[176:177], off offset:-128
	v_lshl_add_u64 v[180:181], s[52:53], 0, v[84:85]
	s_mov_b32 s49, 0x103000
	v_add_co_u32_e32 v182, vcc, s49, v180
	s_mov_b64 s[50:51], 0x103000
	s_nop 0
	v_addc_co_u32_e32 v183, vcc, 0, v181, vcc
	v_lshl_add_u64 v[178:179], v[180:181], 0, s[50:51]
	global_load_dwordx4 v[132:135], v[182:183], off
	global_load_dwordx4 v[136:139], v[178:179], off offset:16
	global_load_dwordx4 v[140:143], v[176:177], off offset:-64
	s_mov_b64 s[50:51], 0x103080
	v_lshl_add_u64 v[178:179], v[180:181], 0, s[50:51]
	global_load_dwordx4 v[144:147], v[182:183], off offset:128
	global_load_dwordx4 v[148:151], v[178:179], off offset:16
	global_load_dwordx4 v[152:155], v[176:177], off
	s_mov_b64 s[50:51], 0x103100
	v_lshl_add_u64 v[178:179], v[180:181], 0, s[50:51]
	s_mov_b64 s[50:51], 0x103180
	v_lshl_add_u64 v[180:181], v[180:181], 0, s[50:51]
	global_load_dwordx4 v[156:159], v[182:183], off offset:256
	global_load_dwordx4 v[160:163], v[178:179], off offset:16
	global_load_dwordx4 v[164:167], v[176:177], off offset:64
	global_load_dwordx4 v[168:171], v[182:183], off offset:384
	global_load_dwordx4 v[172:175], v[180:181], off offset:16
	s_mov_b64 s[50:51], 0x80
.Lrtpf_skip_a:
	v_lshlrev_b32_e32 v90, 16, v44
	v_and_b32_e32 v91, 0xffff0000, v44
	v_pk_mul_f32 v[90:91], v[82:83], v[90:91]
	s_waitcnt lgkmcnt(1)
	v_pk_fma_f32 v[90:91], v[90:91], v[114:115], v[48:49]
	v_lshlrev_b32_e32 v114, 16, v45
	v_and_b32_e32 v115, 0xffff0000, v45
	v_pk_mul_f32 v[114:115], v[82:83], v[114:115]
	v_cvt_pk_bf16_f32 v44, v90, v91
	v_pk_fma_f32 v[114:115], v[114:115], v[116:117], v[50:51]
	v_lshlrev_b32_e32 v48, 16, v44
	v_cvt_pk_bf16_f32 v45, v114, v115
	v_and_b32_e32 v49, 0xffff0000, v44
	v_lshlrev_b32_e32 v50, 16, v45
	v_and_b32_e32 v51, 0xffff0000, v45
	v_pk_add_f32 v[48:49], v[90:91], v[48:49] neg_lo:[0,1] neg_hi:[0,1]
	v_pk_add_f32 v[50:51], v[114:115], v[50:51] neg_lo:[0,1] neg_hi:[0,1]
	v_cvt_pk_bf16_f32 v48, v48, v49
	v_cvt_pk_bf16_f32 v49, v50, v51
	v_lshlrev_b32_e32 v50, 16, v46
	v_and_b32_e32 v51, 0xffff0000, v46
	v_lshlrev_b32_e32 v116, 16, v47
	v_and_b32_e32 v117, 0xffff0000, v47
	v_pk_mul_f32 v[50:51], v[82:83], v[50:51]
	v_pk_mul_f32 v[116:117], v[82:83], v[116:117]
	s_waitcnt lgkmcnt(0)
	v_pk_fma_f32 v[110:111], v[50:51], v[118:119], v[110:111]
	v_pk_fma_f32 v[112:113], v[116:117], v[120:121], v[112:113]
	v_cvt_pk_bf16_f32 v46, v110, v111
	v_cvt_pk_bf16_f32 v47, v112, v113
	v_lshlrev_b32_e32 v50, 16, v46
	v_and_b32_e32 v51, 0xffff0000, v46
	v_lshlrev_b32_e32 v116, 16, v47
	v_and_b32_e32 v117, 0xffff0000, v47
	v_pk_add_f32 v[50:51], v[110:111], v[50:51] neg_lo:[0,1] neg_hi:[0,1]
	v_pk_add_f32 v[116:117], v[112:113], v[116:117] neg_lo:[0,1] neg_hi:[0,1]
	v_cvt_pk_bf16_f32 v50, v50, v51
	v_cvt_pk_bf16_f32 v51, v116, v117
	v_mov_b32_e32 v117, 0
	v_cvt_pk_fp8_f32 v117, v110, v111
	v_mov_b32_e32 v116, 0
	v_cvt_pk_fp8_f32 v116, v90, v91
	v_lshl_add_u64 v[90:91], s[52:53], 0, v[86:87]
	v_cvt_pk_fp8_f32 v117, v112, v113 op_sel:[0,0,1]
	ds_read_b128 v[110:113], v72
	v_cvt_pk_fp8_f32 v116, v114, v115 op_sel:[0,0,1]
	s_waitcnt lgkmcnt(0)
	v_mfma_f32_16x16x32_bf16 v[4:7], v[44:47], v[110:113], v[4:7]
	global_store_dwordx2 v[90:91], v[116:117], off offset:-64
	ds_read_b128 v[114:117], v74
	v_lshl_add_u64 v[86:87], v[86:87], 0, s[50:51]
	v_mfma_f32_16x16x32_bf16 v[4:7], v[48:51], v[110:113], v[4:7]
	ds_read_b128 v[110:113], v72 offset:32768
	v_add_u32_e32 v72, 0x18000, v72
	s_waitcnt lgkmcnt(0)
	v_mfma_f32_16x16x32_bf16 v[0:3], v[44:47], v[110:113], v[0:3]
	v_mfma_f32_16x16x32_bf16 v[4:7], v[44:47], v[114:117], v[4:7]
	ds_read_b128 v[114:117], v72
	v_mfma_f32_16x16x32_bf16 v[0:3], v[48:51], v[110:113], v[0:3]
	v_lshlrev_b32_e32 v110, 16, v32
	v_and_b32_e32 v111, 0xffff0000, v32
	v_add_u32_e32 v48, 0x20090, v70
	s_waitcnt lgkmcnt(0)
	v_mfma_f32_16x16x32_bf16 v[0:3], v[44:47], v[114:117], v[0:3]
	v_add_u32_e32 v44, 0x20080, v70
	ds_read_b128 v[44:47], v44
	ds_read_b128 v[48:51], v48
	v_pk_mul_f32 v[110:111], v[82:83], v[110:111]
	s_waitcnt lgkmcnt(1)
	v_pk_fma_f32 v[44:45], v[110:111], v[44:45], v[40:41]
	v_lshlrev_b32_e32 v110, 16, v33
	v_and_b32_e32 v111, 0xffff0000, v33
	v_pk_mul_f32 v[110:111], v[82:83], v[110:111]
	v_cvt_pk_bf16_f32 v32, v44, v45
	v_pk_fma_f32 v[46:47], v[110:111], v[46:47], v[42:43]
	v_lshlrev_b32_e32 v40, 16, v32
	v_cvt_pk_bf16_f32 v33, v46, v47
	v_and_b32_e32 v41, 0xffff0000, v32
	v_lshlrev_b32_e32 v42, 16, v33
	v_and_b32_e32 v43, 0xffff0000, v33
	v_pk_add_f32 v[40:41], v[44:45], v[40:41] neg_lo:[0,1] neg_hi:[0,1]
	v_pk_add_f32 v[42:43], v[46:47], v[42:43] neg_lo:[0,1] neg_hi:[0,1]
	v_cvt_pk_bf16_f32 v40, v40, v41
	v_cvt_pk_bf16_f32 v41, v42, v43
	v_lshlrev_b32_e32 v42, 16, v34
	v_and_b32_e32 v43, 0xffff0000, v34
	v_pk_mul_f32 v[42:43], v[82:83], v[42:43]
	s_waitcnt lgkmcnt(0)
	v_pk_fma_f32 v[36:37], v[42:43], v[48:49], v[36:37]
	v_lshlrev_b32_e32 v48, 16, v35
	v_and_b32_e32 v49, 0xffff0000, v35
	v_pk_mul_f32 v[48:49], v[82:83], v[48:49]
	v_cvt_pk_bf16_f32 v34, v36, v37
	v_pk_fma_f32 v[38:39], v[48:49], v[50:51], v[38:39]
	v_lshlrev_b32_e32 v42, 16, v34
	v_cvt_pk_bf16_f32 v35, v38, v39
	v_and_b32_e32 v43, 0xffff0000, v34
	v_lshlrev_b32_e32 v48, 16, v35
	v_and_b32_e32 v49, 0xffff0000, v35
	v_pk_add_f32 v[42:43], v[36:37], v[42:43] neg_lo:[0,1] neg_hi:[0,1]
	v_pk_add_f32 v[48:49], v[38:39], v[48:49] neg_lo:[0,1] neg_hi:[0,1]
	v_cvt_pk_bf16_f32 v42, v42, v43
	v_cvt_pk_bf16_f32 v43, v48, v49
	v_mov_b32_e32 v48, 0
	v_mov_b32_e32 v49, 0
	v_cvt_pk_fp8_f32 v48, v44, v45
	v_cvt_pk_fp8_f32 v49, v36, v37
	v_cvt_pk_fp8_f32 v48, v46, v47 op_sel:[0,0,1]
	v_cvt_pk_fp8_f32 v49, v38, v39 op_sel:[0,0,1]
	global_store_dwordx2 v[90:91], v[48:49], off offset:-32
	v_add_u32_e32 v48, 0, v64
	ds_read_b128 v[36:39], v48
	s_waitcnt lgkmcnt(0)
	v_mfma_f32_16x16x32_bf16 v[4:7], v[32:35], v[36:39], v[4:7]
	v_add_u32_e32 v44, 0x10000, v48
	ds_read_b128 v[44:47], v44
	v_add_u32_e32 v64, 0x100, v64
	v_mfma_f32_16x16x32_bf16 v[4:7], v[40:43], v[36:39], v[4:7]
	ds_read_b128 v[36:39], v48 offset:32768
	s_waitcnt lgkmcnt(0)
	v_mfma_f32_16x16x32_bf16 v[0:3], v[32:35], v[36:39], v[0:3]
	v_mfma_f32_16x16x32_bf16 v[4:7], v[32:35], v[44:47], v[4:7]
	v_add_u32_e32 v44, 0x18000, v48
	ds_read_b128 v[44:47], v44
	v_mfma_f32_16x16x32_bf16 v[0:3], v[40:43], v[36:39], v[0:3]
	v_lshlrev_b32_e32 v40, 16, v20
	v_and_b32_e32 v41, 0xffff0000, v20
	v_add_u32_e32 v36, 0x20110, v70
	s_waitcnt lgkmcnt(0)
	v_mfma_f32_16x16x32_bf16 v[0:3], v[32:35], v[44:47], v[0:3]
	v_add_u32_e32 v32, 0x20100, v70
	ds_read_b128 v[32:35], v32
	ds_read_b128 v[36:39], v36
	v_pk_mul_f32 v[40:41], v[82:83], v[40:41]
	s_waitcnt lgkmcnt(1)
	v_pk_fma_f32 v[32:33], v[40:41], v[32:33], v[28:29]
	v_lshlrev_b32_e32 v40, 16, v21
	v_and_b32_e32 v41, 0xffff0000, v21
	v_pk_mul_f32 v[40:41], v[82:83], v[40:41]
	v_cvt_pk_bf16_f32 v20, v32, v33
	v_pk_fma_f32 v[34:35], v[40:41], v[34:35], v[30:31]
	v_lshlrev_b32_e32 v28, 16, v20
	v_cvt_pk_bf16_f32 v21, v34, v35
	v_and_b32_e32 v29, 0xffff0000, v20
	v_lshlrev_b32_e32 v30, 16, v21
	v_and_b32_e32 v31, 0xffff0000, v21
	v_pk_add_f32 v[28:29], v[32:33], v[28:29] neg_lo:[0,1] neg_hi:[0,1]
	v_pk_add_f32 v[30:31], v[34:35], v[30:31] neg_lo:[0,1] neg_hi:[0,1]
	v_cvt_pk_bf16_f32 v28, v28, v29
	v_cvt_pk_bf16_f32 v29, v30, v31
	v_lshlrev_b32_e32 v30, 16, v22
	v_and_b32_e32 v31, 0xffff0000, v22
	v_pk_mul_f32 v[30:31], v[82:83], v[30:31]
	s_waitcnt lgkmcnt(0)
	v_pk_fma_f32 v[24:25], v[30:31], v[36:37], v[24:25]
	v_lshlrev_b32_e32 v36, 16, v23
	v_and_b32_e32 v37, 0xffff0000, v23
	v_pk_mul_f32 v[36:37], v[82:83], v[36:37]
	v_cvt_pk_bf16_f32 v22, v24, v25
	v_pk_fma_f32 v[26:27], v[36:37], v[38:39], v[26:27]
	v_lshlrev_b32_e32 v30, 16, v22
	v_cvt_pk_bf16_f32 v23, v26, v27
	v_and_b32_e32 v31, 0xffff0000, v22
	v_lshlrev_b32_e32 v36, 16, v23
	v_and_b32_e32 v37, 0xffff0000, v23
	v_pk_add_f32 v[30:31], v[24:25], v[30:31] neg_lo:[0,1] neg_hi:[0,1]
	v_pk_add_f32 v[36:37], v[26:27], v[36:37] neg_lo:[0,1] neg_hi:[0,1]
	v_cvt_pk_bf16_f32 v30, v30, v31
	v_cvt_pk_bf16_f32 v31, v36, v37
	v_mov_b32_e32 v36, 0
	v_mov_b32_e32 v37, 0
	v_cvt_pk_fp8_f32 v36, v32, v33
	v_cvt_pk_fp8_f32 v37, v24, v25
	v_cvt_pk_fp8_f32 v36, v34, v35 op_sel:[0,0,1]
	v_cvt_pk_fp8_f32 v37, v26, v27 op_sel:[0,0,1]
	global_store_dwordx2 v[90:91], v[36:37], off
	v_add_u32_e32 v36, 0, v66
	ds_read_b128 v[24:27], v36
	s_waitcnt lgkmcnt(0)
	v_mfma_f32_16x16x32_bf16 v[4:7], v[20:23], v[24:27], v[4:7]
	v_add_u32_e32 v32, 0x10000, v36
	ds_read_b128 v[32:35], v32
	v_add_u32_e32 v66, 0x100, v66
	v_mfma_f32_16x16x32_bf16 v[4:7], v[28:31], v[24:27], v[4:7]
	ds_read_b128 v[24:27], v36 offset:32768
	s_waitcnt lgkmcnt(0)
	v_mfma_f32_16x16x32_bf16 v[0:3], v[20:23], v[24:27], v[0:3]
	v_mfma_f32_16x16x32_bf16 v[4:7], v[20:23], v[32:35], v[4:7]
	v_add_u32_e32 v32, 0x18000, v36
	ds_read_b128 v[32:35], v32
	v_mfma_f32_16x16x32_bf16 v[0:3], v[28:31], v[24:27], v[0:3]
	v_lshlrev_b32_e32 v28, 16, v8
	v_and_b32_e32 v29, 0xffff0000, v8
	v_add_u32_e32 v24, 0x20190, v70
	s_waitcnt lgkmcnt(0)
	v_mfma_f32_16x16x32_bf16 v[0:3], v[20:23], v[32:35], v[0:3]
	v_add_u32_e32 v20, 0x20180, v70
	ds_read_b128 v[20:23], v20
	ds_read_b128 v[24:27], v24
	v_pk_mul_f32 v[28:29], v[82:83], v[28:29]
	s_waitcnt lgkmcnt(1)
	v_pk_fma_f32 v[20:21], v[28:29], v[20:21], v[16:17]
	v_lshlrev_b32_e32 v28, 16, v9
	v_and_b32_e32 v29, 0xffff0000, v9
	v_pk_mul_f32 v[28:29], v[82:83], v[28:29]
	v_cvt_pk_bf16_f32 v8, v20, v21
	v_pk_fma_f32 v[22:23], v[28:29], v[22:23], v[18:19]
	v_lshlrev_b32_e32 v16, 16, v8
	v_cvt_pk_bf16_f32 v9, v22, v23
	v_and_b32_e32 v17, 0xffff0000, v8
	v_lshlrev_b32_e32 v18, 16, v9
	v_and_b32_e32 v19, 0xffff0000, v9
	v_pk_add_f32 v[16:17], v[20:21], v[16:17] neg_lo:[0,1] neg_hi:[0,1]
	v_pk_add_f32 v[18:19], v[22:23], v[18:19] neg_lo:[0,1] neg_hi:[0,1]
	v_cvt_pk_bf16_f32 v16, v16, v17
	v_cvt_pk_bf16_f32 v17, v18, v19
	v_lshlrev_b32_e32 v18, 16, v10
	v_and_b32_e32 v19, 0xffff0000, v10
	v_pk_mul_f32 v[18:19], v[82:83], v[18:19]
	s_waitcnt lgkmcnt(0)
	v_pk_fma_f32 v[12:13], v[18:19], v[24:25], v[12:13]
	v_lshlrev_b32_e32 v24, 16, v11
	v_and_b32_e32 v25, 0xffff0000, v11
	v_pk_mul_f32 v[24:25], v[82:83], v[24:25]
	v_cvt_pk_bf16_f32 v10, v12, v13
	v_pk_fma_f32 v[14:15], v[24:25], v[26:27], v[14:15]
	v_lshlrev_b32_e32 v18, 16, v10
	v_cvt_pk_bf16_f32 v11, v14, v15
	v_and_b32_e32 v19, 0xffff0000, v10
	v_lshlrev_b32_e32 v24, 16, v11
	v_and_b32_e32 v25, 0xffff0000, v11
	v_pk_add_f32 v[18:19], v[12:13], v[18:19] neg_lo:[0,1] neg_hi:[0,1]
	v_pk_add_f32 v[24:25], v[14:15], v[24:25] neg_lo:[0,1] neg_hi:[0,1]
	v_cvt_pk_bf16_f32 v18, v18, v19
	v_cvt_pk_bf16_f32 v19, v24, v25
	v_mov_b32_e32 v24, 0
	v_mov_b32_e32 v25, 0
	v_cvt_pk_fp8_f32 v24, v20, v21
	v_cvt_pk_fp8_f32 v25, v12, v13
	v_cvt_pk_fp8_f32 v24, v22, v23 op_sel:[0,0,1]
	v_cvt_pk_fp8_f32 v25, v14, v15 op_sel:[0,0,1]
	global_store_dwordx2 v[90:91], v[24:25], off offset:32
	v_add_u32_e32 v24, 0, v68
	ds_read_b128 v[12:15], v24
	s_waitcnt lgkmcnt(0)
	v_mfma_f32_16x16x32_bf16 v[4:7], v[8:11], v[12:15], v[4:7]
	v_add_u32_e32 v20, 0x10000, v24
	ds_read_b128 v[20:23], v20
	v_add_u32_e32 v68, 0x100, v68
	v_mfma_f32_16x16x32_bf16 v[4:7], v[16:19], v[12:15], v[4:7]
	ds_read_b128 v[12:15], v24 offset:32768
	s_waitcnt lgkmcnt(0)
	v_mfma_f32_16x16x32_bf16 v[0:3], v[8:11], v[12:15], v[0:3]
	v_mfma_f32_16x16x32_bf16 v[4:7], v[8:11], v[20:23], v[4:7]
	v_add_u32_e32 v20, 0x18000, v24
	ds_read_b128 v[20:23], v20
	v_mfma_f32_16x16x32_bf16 v[0:3], v[16:19], v[12:15], v[0:3]
	s_waitcnt lgkmcnt(0)
	v_mfma_f32_16x16x32_bf16 v[0:3], v[8:11], v[20:23], v[0:3]
	s_cbranch_scc0 .LBB0_581
	global_load_dword v8, v[60:61], off
	global_load_dword v9, v[60:61], off offset:64
	s_waitcnt vmcnt(1)
	v_add_f32_e32 v4, v4, v8
	s_waitcnt vmcnt(0)
	s_nop 1
	v_add_f32_e32 v0, v0, v9
	v_add_f32_e32 v5, v5, v8
	v_add_f32_e32 v6, v6, v8
	v_add_f32_e32 v7, v7, v8
	v_add_f32_e32 v1, v1, v9
	v_add_f32_e32 v2, v2, v9
	v_add_f32_e32 v3, v3, v9
	ds_write2_b32 v95, v4, v0 offset1:16
	ds_write2_b32 v95, v5, v1 offset0:32 offset1:48
	ds_write2_b32 v95, v6, v2 offset0:64 offset1:80
	ds_write2_b32 v95, v7, v3 offset0:96 offset1:112
	ds_read_b128 v[28:31], v107
	ds_read_b128 v[24:27], v107 offset:16
	ds_read_b128 v[20:23], v107 offset:32
	ds_read_b128 v[16:19], v107 offset:48
	ds_read_b128 v[12:15], v107 offset:64
	ds_read_b128 v[8:11], v107 offset:80
	ds_read_b128 v[4:7], v107 offset:96
	ds_read_b128 v[0:3], v107 offset:112
	s_waitcnt lgkmcnt(7)
	v_mov_b32_e32 v52, v28
	s_waitcnt lgkmcnt(3)
	v_mov_b32_e32 v32, v12
	s_and_saveexec_b64 s[48:49], s[6:7]
	s_cbranch_execz .LBB0_588
	v_cmp_lt_i32_e32 vcc, 1, v94
	s_mov_b64 s[54:55], 0
	s_and_saveexec_b64 s[50:51], vcc
	s_xor_b64 s[56:57], exec, s[50:51]
	s_cbranch_execnz .LBB0_655
	s_andn2_saveexec_b64 s[56:57], s[56:57]
	s_cbranch_execnz .LBB0_658

.LBB0_1662:
	s_lshl_b32 s64, s63, 4
	s_add_i32 s48, s64, s60
	v_add_u32_e32 v0, s48, v93
	v_ashrrev_i32_e32 v1, 31, v0
	v_lshlrev_b64 v[0:1], 11, v[0:1]
	v_lshl_add_u64 v[82:83], v[54:55], 0, v[0:1]
	global_load_dwordx4 v[84:87], v[82:83], off
	global_load_dwordx4 v[88:91], v[82:83], off offset:64
	global_load_dwordx4 v[110:113], v[82:83], off offset:128
	global_load_dwordx4 v[48:51], v[82:83], off offset:192
	global_load_dwordx4 v[44:47], v[82:83], off offset:256
	global_load_dwordx4 v[40:43], v[82:83], off offset:320
	global_load_dwordx4 v[36:39], v[82:83], off offset:384
	global_load_dwordx4 v[32:35], v[82:83], off offset:448
	global_load_dwordx4 v[28:31], v[82:83], off offset:512
	global_load_dwordx4 v[24:27], v[82:83], off offset:576
	global_load_dwordx4 v[20:23], v[82:83], off offset:640
	global_load_dwordx4 v[16:19], v[82:83], off offset:704
	global_load_dwordx4 v[12:15], v[82:83], off offset:768
	global_load_dwordx4 v[8:11], v[82:83], off offset:832
	global_load_dwordx4 v[4:7], v[82:83], off offset:896
	global_load_dwordx4 v[0:3], v[82:83], off offset:960
	v_cmp_lt_i32_e32 vcc, v102, v103
	s_mov_b32 s49, 0x800000
	s_min_i32 s48, s48, 0x8000
	s_ashr_i32 s48, s48, 11
	s_cmp_eq_u32 s48, s65
	v_mov_b32_e32 v66, v97
	v_mov_b32_e32 v68, v96
	s_waitcnt vmcnt(15)
	v_and_b32_e32 v62, 0xffff0000, v84
	v_lshlrev_b32_e32 v52, 16, v84
	v_mul_f32_e32 v62, v62, v62
	v_and_b32_e32 v64, 0xffff0000, v85
	v_fmac_f32_e32 v62, v52, v52
	v_lshlrev_b32_e32 v52, 16, v85
	v_mul_f32_e32 v64, v64, v64
	v_fmac_f32_e32 v64, v52, v52
	v_add_f32_e32 v52, v62, v64
	v_and_b32_e32 v64, 0xffff0000, v86
	v_lshlrev_b32_e32 v62, 16, v86
	v_mul_f32_e32 v64, v64, v64
	v_fmac_f32_e32 v64, v62, v62
	v_add_f32_e32 v52, v64, v52
	v_and_b32_e32 v64, 0xffff0000, v87
	v_lshlrev_b32_e32 v62, 16, v87
	v_mul_f32_e32 v64, v64, v64
	v_fmac_f32_e32 v64, v62, v62
	v_add_f32_e32 v52, v64, v52
	s_waitcnt vmcnt(14)
	v_and_b32_e32 v64, 0xffff0000, v88
	v_lshlrev_b32_e32 v62, 16, v88
	v_mul_f32_e32 v64, v64, v64
	v_fmac_f32_e32 v64, v62, v62
	v_add_f32_e32 v52, v64, v52
	v_and_b32_e32 v64, 0xffff0000, v89
	v_lshlrev_b32_e32 v62, 16, v89
	v_mul_f32_e32 v64, v64, v64
	v_fmac_f32_e32 v64, v62, v62
	v_add_f32_e32 v52, v64, v52
	v_and_b32_e32 v64, 0xffff0000, v90
	v_lshlrev_b32_e32 v62, 16, v90
	v_mul_f32_e32 v64, v64, v64
	v_fmac_f32_e32 v64, v62, v62
	v_add_f32_e32 v52, v64, v52
	v_and_b32_e32 v64, 0xffff0000, v91
	v_lshlrev_b32_e32 v62, 16, v91
	v_mul_f32_e32 v64, v64, v64
	v_fmac_f32_e32 v64, v62, v62
	v_add_f32_e32 v52, v64, v52
	s_waitcnt vmcnt(13)
	v_and_b32_e32 v64, 0xffff0000, v110
	v_lshlrev_b32_e32 v62, 16, v110
	v_mul_f32_e32 v64, v64, v64
	v_fmac_f32_e32 v64, v62, v62
	v_add_f32_e32 v52, v64, v52
	v_and_b32_e32 v64, 0xffff0000, v111
	v_lshlrev_b32_e32 v62, 16, v111
	v_mul_f32_e32 v64, v64, v64
	v_fmac_f32_e32 v64, v62, v62
	v_add_f32_e32 v52, v64, v52
	v_and_b32_e32 v64, 0xffff0000, v112
	v_lshlrev_b32_e32 v62, 16, v112
	v_mul_f32_e32 v64, v64, v64
	v_fmac_f32_e32 v64, v62, v62
	v_add_f32_e32 v52, v64, v52
	v_and_b32_e32 v64, 0xffff0000, v113
	v_lshlrev_b32_e32 v62, 16, v113
	v_mul_f32_e32 v64, v64, v64
	v_fmac_f32_e32 v64, v62, v62
	s_waitcnt vmcnt(12)
	v_lshlrev_b32_e32 v62, 16, v48
	v_and_b32_e32 v48, 0xffff0000, v48
	v_mul_f32_e32 v48, v48, v48
	v_add_f32_e32 v52, v64, v52
	v_fmac_f32_e32 v48, v62, v62
	v_add_f32_e32 v48, v48, v52
	v_lshlrev_b32_e32 v52, 16, v49
	v_and_b32_e32 v49, 0xffff0000, v49
	v_mul_f32_e32 v49, v49, v49
	v_fmac_f32_e32 v49, v52, v52
	v_add_f32_e32 v48, v49, v48
	v_lshlrev_b32_e32 v49, 16, v50
	v_and_b32_e32 v50, 0xffff0000, v50
	v_mul_f32_e32 v50, v50, v50
	v_fmac_f32_e32 v50, v49, v49
	v_add_f32_e32 v48, v50, v48
	v_and_b32_e32 v50, 0xffff0000, v51
	v_lshlrev_b32_e32 v49, 16, v51
	v_mul_f32_e32 v50, v50, v50
	v_fmac_f32_e32 v50, v49, v49
	s_waitcnt vmcnt(11)
	v_lshlrev_b32_e32 v49, 16, v44
	v_and_b32_e32 v44, 0xffff0000, v44
	v_mul_f32_e32 v44, v44, v44
	v_add_f32_e32 v48, v50, v48
	v_fmac_f32_e32 v44, v49, v49
	v_add_f32_e32 v44, v44, v48
	v_lshlrev_b32_e32 v48, 16, v45
	v_and_b32_e32 v45, 0xffff0000, v45
	v_mul_f32_e32 v45, v45, v45
	v_fmac_f32_e32 v45, v48, v48
	v_add_f32_e32 v44, v45, v44
	v_lshlrev_b32_e32 v45, 16, v46
	v_and_b32_e32 v46, 0xffff0000, v46
	v_mul_f32_e32 v46, v46, v46
	v_fmac_f32_e32 v46, v45, v45
	v_add_f32_e32 v44, v46, v44
	v_and_b32_e32 v46, 0xffff0000, v47
	v_lshlrev_b32_e32 v45, 16, v47
	v_mul_f32_e32 v46, v46, v46
	v_fmac_f32_e32 v46, v45, v45
	s_waitcnt vmcnt(10)
	v_lshlrev_b32_e32 v45, 16, v40
	v_and_b32_e32 v40, 0xffff0000, v40
	v_mul_f32_e32 v40, v40, v40
	v_add_f32_e32 v44, v46, v44
	v_fmac_f32_e32 v40, v45, v45
	v_add_f32_e32 v40, v40, v44
	v_lshlrev_b32_e32 v44, 16, v41
	v_and_b32_e32 v41, 0xffff0000, v41
	v_mul_f32_e32 v41, v41, v41
	v_fmac_f32_e32 v41, v44, v44
	v_add_f32_e32 v40, v41, v40
	v_lshlrev_b32_e32 v41, 16, v42
	v_and_b32_e32 v42, 0xffff0000, v42
	v_mul_f32_e32 v42, v42, v42
	v_fmac_f32_e32 v42, v41, v41
	v_add_f32_e32 v40, v42, v40
	v_and_b32_e32 v42, 0xffff0000, v43
	v_lshlrev_b32_e32 v41, 16, v43
	v_mul_f32_e32 v42, v42, v42
	v_fmac_f32_e32 v42, v41, v41
	s_waitcnt vmcnt(9)
	v_lshlrev_b32_e32 v41, 16, v36
	v_and_b32_e32 v36, 0xffff0000, v36
	v_mul_f32_e32 v36, v36, v36
	v_add_f32_e32 v40, v42, v40
	v_fmac_f32_e32 v36, v41, v41
	v_add_f32_e32 v36, v36, v40
	v_lshlrev_b32_e32 v40, 16, v37
	v_and_b32_e32 v37, 0xffff0000, v37
	v_mul_f32_e32 v37, v37, v37
	v_fmac_f32_e32 v37, v40, v40
	v_add_f32_e32 v36, v37, v36
	v_lshlrev_b32_e32 v37, 16, v38
	v_and_b32_e32 v38, 0xffff0000, v38
	v_mul_f32_e32 v38, v38, v38
	v_fmac_f32_e32 v38, v37, v37
	v_add_f32_e32 v36, v38, v36
	v_and_b32_e32 v38, 0xffff0000, v39
	v_lshlrev_b32_e32 v37, 16, v39
	v_mul_f32_e32 v38, v38, v38
	v_fmac_f32_e32 v38, v37, v37
	s_waitcnt vmcnt(8)
	v_lshlrev_b32_e32 v37, 16, v32
	v_and_b32_e32 v32, 0xffff0000, v32
	v_mul_f32_e32 v32, v32, v32
	v_add_f32_e32 v36, v38, v36
	v_fmac_f32_e32 v32, v37, v37
	v_add_f32_e32 v32, v32, v36
	v_lshlrev_b32_e32 v36, 16, v33
	v_and_b32_e32 v33, 0xffff0000, v33
	v_mul_f32_e32 v33, v33, v33
	v_fmac_f32_e32 v33, v36, v36
	v_add_f32_e32 v32, v33, v32
	v_lshlrev_b32_e32 v33, 16, v34
	v_and_b32_e32 v34, 0xffff0000, v34
	v_mul_f32_e32 v34, v34, v34
	v_fmac_f32_e32 v34, v33, v33
	v_add_f32_e32 v32, v34, v32
	v_and_b32_e32 v34, 0xffff0000, v35
	v_lshlrev_b32_e32 v33, 16, v35
	v_mul_f32_e32 v34, v34, v34
	v_fmac_f32_e32 v34, v33, v33
	s_waitcnt vmcnt(7)
	v_lshlrev_b32_e32 v33, 16, v28
	v_and_b32_e32 v28, 0xffff0000, v28
	v_mul_f32_e32 v28, v28, v28
	v_add_f32_e32 v32, v34, v32
	v_fmac_f32_e32 v28, v33, v33
	v_add_f32_e32 v28, v28, v32
	v_lshlrev_b32_e32 v32, 16, v29
	v_and_b32_e32 v29, 0xffff0000, v29
	v_mul_f32_e32 v29, v29, v29
	v_fmac_f32_e32 v29, v32, v32
	v_add_f32_e32 v28, v29, v28
	v_lshlrev_b32_e32 v29, 16, v30
	v_and_b32_e32 v30, 0xffff0000, v30
	v_mul_f32_e32 v30, v30, v30
	v_fmac_f32_e32 v30, v29, v29
	v_add_f32_e32 v28, v30, v28
	v_and_b32_e32 v30, 0xffff0000, v31
	v_lshlrev_b32_e32 v29, 16, v31
	v_mul_f32_e32 v30, v30, v30
	v_fmac_f32_e32 v30, v29, v29
	s_waitcnt vmcnt(6)
	v_lshlrev_b32_e32 v29, 16, v24
	v_and_b32_e32 v24, 0xffff0000, v24
	v_mul_f32_e32 v24, v24, v24
	v_add_f32_e32 v28, v30, v28
	v_fmac_f32_e32 v24, v29, v29
	v_add_f32_e32 v24, v24, v28
	v_lshlrev_b32_e32 v28, 16, v25
	v_and_b32_e32 v25, 0xffff0000, v25
	v_mul_f32_e32 v25, v25, v25
	v_fmac_f32_e32 v25, v28, v28
	v_add_f32_e32 v24, v25, v24
	v_lshlrev_b32_e32 v25, 16, v26
	v_and_b32_e32 v26, 0xffff0000, v26
	v_mul_f32_e32 v26, v26, v26
	v_fmac_f32_e32 v26, v25, v25
	v_add_f32_e32 v24, v26, v24
	v_and_b32_e32 v26, 0xffff0000, v27
	v_lshlrev_b32_e32 v25, 16, v27
	v_mul_f32_e32 v26, v26, v26
	v_fmac_f32_e32 v26, v25, v25
	s_waitcnt vmcnt(5)
	v_lshlrev_b32_e32 v25, 16, v20
	v_and_b32_e32 v20, 0xffff0000, v20
	v_mul_f32_e32 v20, v20, v20
	v_add_f32_e32 v24, v26, v24
	v_fmac_f32_e32 v20, v25, v25
	v_add_f32_e32 v20, v20, v24
	v_lshlrev_b32_e32 v24, 16, v21
	v_and_b32_e32 v21, 0xffff0000, v21
	v_mul_f32_e32 v21, v21, v21
	v_fmac_f32_e32 v21, v24, v24
	v_add_f32_e32 v20, v21, v20
	v_lshlrev_b32_e32 v21, 16, v22
	v_and_b32_e32 v22, 0xffff0000, v22
	v_mul_f32_e32 v22, v22, v22
	v_fmac_f32_e32 v22, v21, v21
	v_add_f32_e32 v20, v22, v20
	v_and_b32_e32 v22, 0xffff0000, v23
	v_lshlrev_b32_e32 v21, 16, v23
	v_mul_f32_e32 v22, v22, v22
	v_fmac_f32_e32 v22, v21, v21
	s_waitcnt vmcnt(4)
	v_lshlrev_b32_e32 v21, 16, v16
	v_and_b32_e32 v16, 0xffff0000, v16
	v_mul_f32_e32 v16, v16, v16
	v_add_f32_e32 v20, v22, v20
	v_fmac_f32_e32 v16, v21, v21
	v_add_f32_e32 v16, v16, v20
	v_lshlrev_b32_e32 v20, 16, v17
	v_and_b32_e32 v17, 0xffff0000, v17
	v_mul_f32_e32 v17, v17, v17
	v_fmac_f32_e32 v17, v20, v20
	v_add_f32_e32 v16, v17, v16
	v_lshlrev_b32_e32 v17, 16, v18
	v_and_b32_e32 v18, 0xffff0000, v18
	v_mul_f32_e32 v18, v18, v18
	v_fmac_f32_e32 v18, v17, v17
	v_add_f32_e32 v16, v18, v16
	v_and_b32_e32 v18, 0xffff0000, v19
	v_lshlrev_b32_e32 v17, 16, v19
	v_mul_f32_e32 v18, v18, v18
	v_fmac_f32_e32 v18, v17, v17
	s_waitcnt vmcnt(3)
	v_lshlrev_b32_e32 v17, 16, v12
	v_and_b32_e32 v12, 0xffff0000, v12
	v_mul_f32_e32 v12, v12, v12
	v_add_f32_e32 v16, v18, v16
	v_fmac_f32_e32 v12, v17, v17
	v_add_f32_e32 v12, v12, v16
	v_lshlrev_b32_e32 v16, 16, v13
	v_and_b32_e32 v13, 0xffff0000, v13
	v_mul_f32_e32 v13, v13, v13
	v_fmac_f32_e32 v13, v16, v16
	v_add_f32_e32 v12, v13, v12
	v_lshlrev_b32_e32 v13, 16, v14
	v_and_b32_e32 v14, 0xffff0000, v14
	v_mul_f32_e32 v14, v14, v14
	v_fmac_f32_e32 v14, v13, v13
	v_add_f32_e32 v12, v14, v12
	v_and_b32_e32 v14, 0xffff0000, v15
	v_lshlrev_b32_e32 v13, 16, v15
	v_mul_f32_e32 v14, v14, v14
	v_fmac_f32_e32 v14, v13, v13
	s_waitcnt vmcnt(2)
	v_lshlrev_b32_e32 v13, 16, v8
	v_and_b32_e32 v8, 0xffff0000, v8
	v_mul_f32_e32 v8, v8, v8
	v_add_f32_e32 v12, v14, v12
	v_fmac_f32_e32 v8, v13, v13
	v_add_f32_e32 v8, v8, v12
	v_lshlrev_b32_e32 v12, 16, v9
	v_and_b32_e32 v9, 0xffff0000, v9
	v_mul_f32_e32 v9, v9, v9
	v_fmac_f32_e32 v9, v12, v12
	v_add_f32_e32 v8, v9, v8
	v_lshlrev_b32_e32 v9, 16, v10
	v_and_b32_e32 v10, 0xffff0000, v10
	v_mul_f32_e32 v10, v10, v10
	v_fmac_f32_e32 v10, v9, v9
	v_add_f32_e32 v8, v10, v8
	v_and_b32_e32 v10, 0xffff0000, v11
	v_lshlrev_b32_e32 v9, 16, v11
	v_mul_f32_e32 v10, v10, v10
	v_fmac_f32_e32 v10, v9, v9
	s_waitcnt vmcnt(1)
	v_lshlrev_b32_e32 v9, 16, v4
	v_and_b32_e32 v4, 0xffff0000, v4
	v_mul_f32_e32 v4, v4, v4
	v_add_f32_e32 v8, v10, v8
	v_fmac_f32_e32 v4, v9, v9
	v_add_f32_e32 v4, v4, v8
	v_lshlrev_b32_e32 v8, 16, v5
	v_and_b32_e32 v5, 0xffff0000, v5
	v_mul_f32_e32 v5, v5, v5
	v_fmac_f32_e32 v5, v8, v8
	v_add_f32_e32 v4, v5, v4
	v_lshlrev_b32_e32 v5, 16, v6
	v_and_b32_e32 v6, 0xffff0000, v6
	v_mul_f32_e32 v6, v6, v6
	v_fmac_f32_e32 v6, v5, v5
	v_add_f32_e32 v4, v6, v4
	v_and_b32_e32 v6, 0xffff0000, v7
	v_lshlrev_b32_e32 v5, 16, v7
	v_mul_f32_e32 v6, v6, v6
	v_fmac_f32_e32 v6, v5, v5
	s_waitcnt vmcnt(0)
	v_lshlrev_b32_e32 v5, 16, v0
	v_and_b32_e32 v0, 0xffff0000, v0
	v_mul_f32_e32 v0, v0, v0
	v_add_f32_e32 v4, v6, v4
	v_fmac_f32_e32 v0, v5, v5
	v_add_f32_e32 v0, v0, v4
	v_lshlrev_b32_e32 v4, 16, v1
	v_and_b32_e32 v1, 0xffff0000, v1
	v_mul_f32_e32 v1, v1, v1
	v_fmac_f32_e32 v1, v4, v4
	v_add_f32_e32 v0, v1, v0
	v_lshlrev_b32_e32 v1, 16, v2
	v_and_b32_e32 v2, 0xffff0000, v2
	v_mul_f32_e32 v2, v2, v2
	v_fmac_f32_e32 v2, v1, v1
	v_add_f32_e32 v0, v2, v0
	v_and_b32_e32 v2, 0xffff0000, v3
	v_lshlrev_b32_e32 v1, 16, v3
	v_mul_f32_e32 v2, v2, v2
	v_fmac_f32_e32 v2, v1, v1
	v_add_f32_e32 v28, v2, v0
	global_load_dwordx4 v[16:19], v[82:83], off offset:1024
	global_load_dwordx4 v[30:33], v[82:83], off offset:1088
	global_load_dwordx4 v[34:37], v[82:83], off offset:1152
	global_load_dwordx4 v[38:41], v[82:83], off offset:1216
	global_load_dwordx4 v[42:45], v[82:83], off offset:1280
	global_load_dwordx4 v[46:49], v[82:83], off offset:1344
	global_load_dwordx4 v[84:87], v[82:83], off offset:1408
	global_load_dwordx4 v[88:91], v[82:83], off offset:1472
	global_load_dwordx4 v[110:113], v[82:83], off offset:1536
	global_load_dwordx4 v[114:117], v[82:83], off offset:1600
	global_load_dwordx4 v[24:27], v[82:83], off offset:1664
	global_load_dwordx4 v[20:23], v[82:83], off offset:1728
	global_load_dwordx4 v[12:15], v[82:83], off offset:1792
	global_load_dwordx4 v[8:11], v[82:83], off offset:1856
	global_load_dwordx4 v[4:7], v[82:83], off offset:1920
	global_load_dwordx4 v[0:3], v[82:83], off offset:1984
	v_mov_b32_e32 v62, v99
	v_mov_b32_e32 v64, v98
	s_waitcnt vmcnt(15)
	v_lshlrev_b32_e32 v29, 16, v16
	v_and_b32_e32 v16, 0xffff0000, v16
	v_mul_f32_e32 v16, v16, v16
	v_fmac_f32_e32 v16, v29, v29
	v_add_f32_e32 v16, v16, v28
	v_lshlrev_b32_e32 v28, 16, v17
	v_and_b32_e32 v17, 0xffff0000, v17
	v_mul_f32_e32 v17, v17, v17
	v_fmac_f32_e32 v17, v28, v28
	v_add_f32_e32 v16, v17, v16
	v_lshlrev_b32_e32 v17, 16, v18
	v_and_b32_e32 v18, 0xffff0000, v18
	v_mul_f32_e32 v18, v18, v18
	v_fmac_f32_e32 v18, v17, v17
	v_add_f32_e32 v16, v18, v16
	v_and_b32_e32 v18, 0xffff0000, v19
	v_lshlrev_b32_e32 v17, 16, v19
	v_mul_f32_e32 v18, v18, v18
	v_fmac_f32_e32 v18, v17, v17
	v_add_f32_e32 v16, v18, v16
	s_waitcnt vmcnt(14)
	v_and_b32_e32 v18, 0xffff0000, v30
	v_lshlrev_b32_e32 v17, 16, v30
	v_mul_f32_e32 v18, v18, v18
	v_fmac_f32_e32 v18, v17, v17
	v_add_f32_e32 v16, v18, v16
	v_and_b32_e32 v18, 0xffff0000, v31
	v_lshlrev_b32_e32 v17, 16, v31
	v_mul_f32_e32 v18, v18, v18
	v_fmac_f32_e32 v18, v17, v17
	v_add_f32_e32 v16, v18, v16
	v_and_b32_e32 v18, 0xffff0000, v32
	v_lshlrev_b32_e32 v17, 16, v32
	v_mul_f32_e32 v18, v18, v18
	v_fmac_f32_e32 v18, v17, v17
	v_add_f32_e32 v16, v18, v16
	v_and_b32_e32 v18, 0xffff0000, v33
	v_lshlrev_b32_e32 v17, 16, v33
	v_mul_f32_e32 v18, v18, v18
	v_fmac_f32_e32 v18, v17, v17
	v_add_f32_e32 v16, v18, v16
	s_waitcnt vmcnt(13)
	v_and_b32_e32 v18, 0xffff0000, v34
	v_lshlrev_b32_e32 v17, 16, v34
	v_mul_f32_e32 v18, v18, v18
	v_fmac_f32_e32 v18, v17, v17
	v_add_f32_e32 v16, v18, v16
	v_and_b32_e32 v18, 0xffff0000, v35
	v_lshlrev_b32_e32 v17, 16, v35
	v_mul_f32_e32 v18, v18, v18
	v_fmac_f32_e32 v18, v17, v17
	v_add_f32_e32 v16, v18, v16
	v_and_b32_e32 v18, 0xffff0000, v36
	v_lshlrev_b32_e32 v17, 16, v36
	v_mul_f32_e32 v18, v18, v18
	v_fmac_f32_e32 v18, v17, v17
	v_add_f32_e32 v16, v18, v16
	v_and_b32_e32 v18, 0xffff0000, v37
	v_lshlrev_b32_e32 v17, 16, v37
	v_mul_f32_e32 v18, v18, v18
	v_fmac_f32_e32 v18, v17, v17
	v_add_f32_e32 v16, v18, v16
	s_waitcnt vmcnt(12)
	v_and_b32_e32 v18, 0xffff0000, v38
	v_lshlrev_b32_e32 v17, 16, v38
	v_mul_f32_e32 v18, v18, v18
	v_fmac_f32_e32 v18, v17, v17
	v_add_f32_e32 v16, v18, v16
	v_and_b32_e32 v18, 0xffff0000, v39
	v_lshlrev_b32_e32 v17, 16, v39
	v_mul_f32_e32 v18, v18, v18
	v_fmac_f32_e32 v18, v17, v17
	v_add_f32_e32 v16, v18, v16
	v_and_b32_e32 v18, 0xffff0000, v40
	v_lshlrev_b32_e32 v17, 16, v40
	v_mul_f32_e32 v18, v18, v18
	v_fmac_f32_e32 v18, v17, v17
	v_add_f32_e32 v16, v18, v16
	v_and_b32_e32 v18, 0xffff0000, v41
	v_lshlrev_b32_e32 v17, 16, v41
	v_mul_f32_e32 v18, v18, v18
	v_fmac_f32_e32 v18, v17, v17
	v_add_f32_e32 v16, v18, v16
	s_waitcnt vmcnt(11)
	v_and_b32_e32 v18, 0xffff0000, v42
	v_lshlrev_b32_e32 v17, 16, v42
	v_mul_f32_e32 v18, v18, v18
	v_fmac_f32_e32 v18, v17, v17
	v_add_f32_e32 v16, v18, v16
	v_and_b32_e32 v18, 0xffff0000, v43
	v_lshlrev_b32_e32 v17, 16, v43
	v_mul_f32_e32 v18, v18, v18
	v_fmac_f32_e32 v18, v17, v17
	v_add_f32_e32 v16, v18, v16
	v_and_b32_e32 v18, 0xffff0000, v44
	v_lshlrev_b32_e32 v17, 16, v44
	v_mul_f32_e32 v18, v18, v18
	v_fmac_f32_e32 v18, v17, v17
	v_add_f32_e32 v16, v18, v16
	v_and_b32_e32 v18, 0xffff0000, v45
	v_lshlrev_b32_e32 v17, 16, v45
	v_mul_f32_e32 v18, v18, v18
	v_fmac_f32_e32 v18, v17, v17
	v_add_f32_e32 v16, v18, v16
	s_waitcnt vmcnt(10)
	v_and_b32_e32 v18, 0xffff0000, v46
	v_lshlrev_b32_e32 v17, 16, v46
	v_mul_f32_e32 v18, v18, v18
	v_fmac_f32_e32 v18, v17, v17
	v_add_f32_e32 v16, v18, v16
	v_and_b32_e32 v18, 0xffff0000, v47
	v_lshlrev_b32_e32 v17, 16, v47
	v_mul_f32_e32 v18, v18, v18
	v_fmac_f32_e32 v18, v17, v17
	v_add_f32_e32 v16, v18, v16
	v_and_b32_e32 v18, 0xffff0000, v48
	v_lshlrev_b32_e32 v17, 16, v48
	v_mul_f32_e32 v18, v18, v18
	v_fmac_f32_e32 v18, v17, v17
	v_add_f32_e32 v16, v18, v16
	v_and_b32_e32 v18, 0xffff0000, v49
	v_lshlrev_b32_e32 v17, 16, v49
	v_mul_f32_e32 v18, v18, v18
	v_fmac_f32_e32 v18, v17, v17
	v_add_f32_e32 v16, v18, v16
	s_waitcnt vmcnt(9)
	v_and_b32_e32 v18, 0xffff0000, v84
	v_lshlrev_b32_e32 v17, 16, v84
	v_mul_f32_e32 v18, v18, v18
	v_fmac_f32_e32 v18, v17, v17
	v_add_f32_e32 v16, v18, v16
	v_and_b32_e32 v18, 0xffff0000, v85
	v_lshlrev_b32_e32 v17, 16, v85
	v_mul_f32_e32 v18, v18, v18
	v_fmac_f32_e32 v18, v17, v17
	v_add_f32_e32 v16, v18, v16
	v_and_b32_e32 v18, 0xffff0000, v86
	v_lshlrev_b32_e32 v17, 16, v86
	v_mul_f32_e32 v18, v18, v18
	v_fmac_f32_e32 v18, v17, v17
	v_add_f32_e32 v16, v18, v16
	v_and_b32_e32 v18, 0xffff0000, v87
	v_lshlrev_b32_e32 v17, 16, v87
	v_mul_f32_e32 v18, v18, v18
	v_fmac_f32_e32 v18, v17, v17
	v_add_f32_e32 v16, v18, v16
	s_waitcnt vmcnt(8)
	v_and_b32_e32 v18, 0xffff0000, v88
	v_lshlrev_b32_e32 v17, 16, v88
	v_mul_f32_e32 v18, v18, v18
	v_fmac_f32_e32 v18, v17, v17
	v_add_f32_e32 v16, v18, v16
	v_and_b32_e32 v18, 0xffff0000, v89
	v_lshlrev_b32_e32 v17, 16, v89
	v_mul_f32_e32 v18, v18, v18
	v_fmac_f32_e32 v18, v17, v17
	v_add_f32_e32 v16, v18, v16
	v_and_b32_e32 v18, 0xffff0000, v90
	v_lshlrev_b32_e32 v17, 16, v90
	v_mul_f32_e32 v18, v18, v18
	v_fmac_f32_e32 v18, v17, v17
	v_add_f32_e32 v16, v18, v16
	v_and_b32_e32 v18, 0xffff0000, v91
	v_lshlrev_b32_e32 v17, 16, v91
	v_mul_f32_e32 v18, v18, v18
	v_fmac_f32_e32 v18, v17, v17
	v_add_f32_e32 v16, v18, v16
	s_waitcnt vmcnt(7)
	v_and_b32_e32 v18, 0xffff0000, v110
	v_lshlrev_b32_e32 v17, 16, v110
	v_mul_f32_e32 v18, v18, v18
	v_fmac_f32_e32 v18, v17, v17
	v_add_f32_e32 v16, v18, v16
	v_and_b32_e32 v18, 0xffff0000, v111
	v_lshlrev_b32_e32 v17, 16, v111
	v_mul_f32_e32 v18, v18, v18
	v_fmac_f32_e32 v18, v17, v17
	v_add_f32_e32 v16, v18, v16
	v_and_b32_e32 v18, 0xffff0000, v112
	v_lshlrev_b32_e32 v17, 16, v112
	v_mul_f32_e32 v18, v18, v18
	v_fmac_f32_e32 v18, v17, v17
	v_add_f32_e32 v16, v18, v16
	v_and_b32_e32 v18, 0xffff0000, v113
	v_lshlrev_b32_e32 v17, 16, v113
	v_mul_f32_e32 v18, v18, v18
	v_fmac_f32_e32 v18, v17, v17
	v_add_f32_e32 v16, v18, v16
	s_waitcnt vmcnt(6)
	v_and_b32_e32 v18, 0xffff0000, v114
	v_lshlrev_b32_e32 v17, 16, v114
	v_mul_f32_e32 v18, v18, v18
	v_fmac_f32_e32 v18, v17, v17
	v_add_f32_e32 v16, v18, v16
	v_and_b32_e32 v18, 0xffff0000, v115
	v_lshlrev_b32_e32 v17, 16, v115
	v_mul_f32_e32 v18, v18, v18
	v_fmac_f32_e32 v18, v17, v17
	v_add_f32_e32 v16, v18, v16
	v_and_b32_e32 v18, 0xffff0000, v116
	v_lshlrev_b32_e32 v17, 16, v116
	v_mul_f32_e32 v18, v18, v18
	v_fmac_f32_e32 v18, v17, v17
	v_add_f32_e32 v16, v18, v16
	v_and_b32_e32 v18, 0xffff0000, v117
	v_lshlrev_b32_e32 v17, 16, v117
	v_mul_f32_e32 v18, v18, v18
	v_fmac_f32_e32 v18, v17, v17
	v_add_f32_e32 v16, v18, v16
	s_waitcnt vmcnt(5)
	v_and_b32_e32 v18, 0xffff0000, v24
	v_lshlrev_b32_e32 v17, 16, v24
	v_mul_f32_e32 v18, v18, v18
	v_fmac_f32_e32 v18, v17, v17
	v_add_f32_e32 v16, v18, v16
	v_and_b32_e32 v18, 0xffff0000, v25
	v_lshlrev_b32_e32 v17, 16, v25
	v_mul_f32_e32 v18, v18, v18
	v_fmac_f32_e32 v18, v17, v17
	v_add_f32_e32 v16, v18, v16
	v_and_b32_e32 v18, 0xffff0000, v26
	v_lshlrev_b32_e32 v17, 16, v26
	v_mul_f32_e32 v18, v18, v18
	v_fmac_f32_e32 v18, v17, v17
	v_add_f32_e32 v16, v18, v16
	v_and_b32_e32 v18, 0xffff0000, v27
	v_lshlrev_b32_e32 v17, 16, v27
	v_mul_f32_e32 v18, v18, v18
	v_fmac_f32_e32 v18, v17, v17
	v_add_f32_e32 v16, v18, v16
	s_waitcnt vmcnt(4)
	v_and_b32_e32 v18, 0xffff0000, v20
	v_lshlrev_b32_e32 v17, 16, v20
	v_mul_f32_e32 v18, v18, v18
	v_fmac_f32_e32 v18, v17, v17
	v_add_f32_e32 v16, v18, v16
	v_and_b32_e32 v18, 0xffff0000, v21
	v_lshlrev_b32_e32 v17, 16, v21
	v_mul_f32_e32 v18, v18, v18
	v_fmac_f32_e32 v18, v17, v17
	v_add_f32_e32 v16, v18, v16
	v_and_b32_e32 v18, 0xffff0000, v22
	v_lshlrev_b32_e32 v17, 16, v22
	v_mul_f32_e32 v18, v18, v18
	v_fmac_f32_e32 v18, v17, v17
	v_add_f32_e32 v16, v18, v16
	v_and_b32_e32 v18, 0xffff0000, v23
	v_lshlrev_b32_e32 v17, 16, v23
	v_mul_f32_e32 v18, v18, v18
	v_fmac_f32_e32 v18, v17, v17
	s_waitcnt vmcnt(3)
	v_lshlrev_b32_e32 v17, 16, v12
	v_and_b32_e32 v12, 0xffff0000, v12
	v_mul_f32_e32 v12, v12, v12
	v_add_f32_e32 v16, v18, v16
	v_fmac_f32_e32 v12, v17, v17
	v_add_f32_e32 v12, v12, v16
	v_lshlrev_b32_e32 v16, 16, v13
	v_and_b32_e32 v13, 0xffff0000, v13
	v_mul_f32_e32 v13, v13, v13
	v_fmac_f32_e32 v13, v16, v16
	v_add_f32_e32 v12, v13, v12
	v_lshlrev_b32_e32 v13, 16, v14
	v_and_b32_e32 v14, 0xffff0000, v14
	v_mul_f32_e32 v14, v14, v14
	v_fmac_f32_e32 v14, v13, v13
	v_add_f32_e32 v12, v14, v12
	v_and_b32_e32 v14, 0xffff0000, v15
	v_lshlrev_b32_e32 v13, 16, v15
	v_mul_f32_e32 v14, v14, v14
	v_fmac_f32_e32 v14, v13, v13
	s_waitcnt vmcnt(2)
	v_lshlrev_b32_e32 v13, 16, v8
	v_and_b32_e32 v8, 0xffff0000, v8
	v_mul_f32_e32 v8, v8, v8
	v_add_f32_e32 v12, v14, v12
	v_fmac_f32_e32 v8, v13, v13
	v_add_f32_e32 v8, v8, v12
	v_lshlrev_b32_e32 v12, 16, v9
	v_and_b32_e32 v9, 0xffff0000, v9
	v_mul_f32_e32 v9, v9, v9
	v_fmac_f32_e32 v9, v12, v12
	v_add_f32_e32 v8, v9, v8
	v_lshlrev_b32_e32 v9, 16, v10
	v_and_b32_e32 v10, 0xffff0000, v10
	v_mul_f32_e32 v10, v10, v10
	v_fmac_f32_e32 v10, v9, v9
	v_add_f32_e32 v8, v10, v8
	v_and_b32_e32 v10, 0xffff0000, v11
	v_lshlrev_b32_e32 v9, 16, v11
	v_mul_f32_e32 v10, v10, v10
	v_fmac_f32_e32 v10, v9, v9
	v_add_f32_e32 v10, v10, v8
	s_waitcnt vmcnt(1)
	v_lshlrev_b32_e32 v9, 16, v5
	v_lshlrev_b32_e32 v8, 16, v4
	v_and_b32_e32 v5, 0xffff0000, v5
	v_and_b32_e32 v4, 0xffff0000, v4
	v_pk_mul_f32 v[4:5], v[4:5], v[4:5]
	v_mov_b64_e32 v[86:87], v[80:81]
	v_pk_fma_f32 v[4:5], v[8:9], v[8:9], v[4:5]
	v_mov_b64_e32 v[88:89], v[76:77]
	v_add_f32_e32 v4, v4, v10
	v_add_f32_e32 v8, v5, v4
	v_lshlrev_b32_e32 v5, 16, v7
	v_lshlrev_b32_e32 v4, 16, v6
	v_and_b32_e32 v7, 0xffff0000, v7
	v_and_b32_e32 v6, 0xffff0000, v6
	v_pk_mul_f32 v[6:7], v[6:7], v[6:7]
	s_nop 0
	v_pk_fma_f32 v[4:5], v[4:5], v[4:5], v[6:7]
	v_mov_b32_e32 v7, v59
	v_add_f32_e32 v4, v4, v8
	v_add_f32_e32 v6, v5, v4
	s_waitcnt vmcnt(0)
	v_lshlrev_b32_e32 v5, 16, v1
	v_lshlrev_b32_e32 v4, 16, v0
	v_and_b32_e32 v1, 0xffff0000, v1
	v_and_b32_e32 v0, 0xffff0000, v0
	v_pk_mul_f32 v[0:1], v[0:1], v[0:1]
	s_nop 0
	v_pk_fma_f32 v[0:1], v[4:5], v[4:5], v[0:1]
	v_mov_b32_e32 v5, v59
	v_add_f32_e32 v0, v0, v6
	v_add_f32_e32 v4, v1, v0
	v_lshlrev_b32_e32 v1, 16, v3
	v_lshlrev_b32_e32 v0, 16, v2
	v_and_b32_e32 v3, 0xffff0000, v3
	v_and_b32_e32 v2, 0xffff0000, v2
	v_pk_mul_f32 v[2:3], v[2:3], v[2:3]
	v_mov_b32_e32 v6, v59
	v_pk_fma_f32 v[0:1], v[0:1], v[0:1], v[2:3]
	v_mov_b32_e32 v2, v59
	v_add_f32_e32 v0, v0, v4
	v_add_f32_e32 v0, v1, v0
	v_cndmask_b32_e32 v1, v101, v102, vcc
	v_lshlrev_b32_e32 v1, 2, v1
	ds_bpermute_b32 v1, v1, v0
	v_cmp_lt_i32_e32 vcc, v104, v103
	v_mov_b32_e32 v4, 0
	v_mov_b32_e32 v3, v59
	s_waitcnt lgkmcnt(0)
	v_add_f32_e32 v0, v0, v1
	v_cndmask_b32_e32 v1, v101, v104, vcc
	v_lshlrev_b32_e32 v1, 2, v1
	ds_bpermute_b32 v1, v1, v0
	s_waitcnt lgkmcnt(0)
	v_add_f32_e32 v0, v0, v1
	v_fmamk_f32 v0, v0, 0x3a800000, v105
	v_cmp_gt_f32_e32 vcc, s49, v0
	v_mul_f32_e32 v1, 0x4b800000, v0
	s_cselect_b32 s49, 0, 0x1000
	v_cndmask_b32_e32 v0, v0, v1, vcc
	v_rsq_f32_e32 v0, v0
	v_add_u32_e32 v52, s49, v100
	v_mad_i64_i32 v[84:85], s[48:49], s48, v106, v[78:79]
	v_mul_f32_e32 v1, 0x45800000, v0
	v_cndmask_b32_e32 v82, v0, v1, vcc
	v_mov_b32_e32 v83, v82
	s_mov_b32 s48, 8
	v_mov_b32_e32 v0, 0
	v_mov_b32_e32 v1, v59
	v_lshl_add_u64 v[176:177], s[52:53], 0, v[88:89]
	global_load_dwordx4 v[128:131], v[176:177], off offset:-128
	v_lshl_add_u64 v[180:181], s[52:53], 0, v[84:85]
	s_mov_b32 s49, 0x169000
	v_add_co_u32_e32 v182, vcc, s49, v180
	s_mov_b64 s[50:51], 0x169000
	s_nop 0
	v_addc_co_u32_e32 v183, vcc, 0, v181, vcc
	v_lshl_add_u64 v[178:179], v[180:181], 0, s[50:51]
	global_load_dwordx4 v[132:135], v[182:183], off
	global_load_dwordx4 v[136:139], v[178:179], off offset:16
	global_load_dwordx4 v[140:143], v[176:177], off offset:-64
	s_mov_b64 s[50:51], 0x169080
	v_lshl_add_u64 v[178:179], v[180:181], 0, s[50:51]
	global_load_dwordx4 v[144:147], v[182:183], off offset:128
	global_load_dwordx4 v[148:151], v[178:179], off offset:16
	global_load_dwordx4 v[152:155], v[176:177], off
	s_mov_b64 s[50:51], 0x169100
	v_lshl_add_u64 v[178:179], v[180:181], 0, s[50:51]
	s_mov_b64 s[50:51], 0x169180
	v_lshl_add_u64 v[180:181], v[180:181], 0, s[50:51]
	global_load_dwordx4 v[156:159], v[182:183], off offset:256
	global_load_dwordx4 v[160:163], v[178:179], off offset:16
	global_load_dwordx4 v[164:167], v[176:177], off offset:64
	global_load_dwordx4 v[168:171], v[182:183], off offset:384
	global_load_dwordx4 v[172:175], v[180:181], off offset:16
.LBB0_1663:
	s_waitcnt vmcnt(0)
	v_mov_b64_e32 v[44:45], v[128:129]
	v_mov_b64_e32 v[46:47], v[130:131]
	v_mov_b64_e32 v[48:49], v[132:133]
	v_mov_b64_e32 v[50:51], v[134:135]
	v_mov_b64_e32 v[110:111], v[136:137]
	v_mov_b64_e32 v[112:113], v[138:139]
	v_mov_b64_e32 v[32:33], v[140:141]
	v_mov_b64_e32 v[34:35], v[142:143]
	v_mov_b64_e32 v[40:41], v[144:145]
	v_mov_b64_e32 v[42:43], v[146:147]
	v_mov_b64_e32 v[36:37], v[148:149]
	v_mov_b64_e32 v[38:39], v[150:151]
	v_mov_b64_e32 v[20:21], v[152:153]
	v_mov_b64_e32 v[22:23], v[154:155]
	v_mov_b64_e32 v[28:29], v[156:157]
	v_mov_b64_e32 v[30:31], v[158:159]
	v_mov_b64_e32 v[24:25], v[160:161]
	v_mov_b64_e32 v[26:27], v[162:163]
	v_mov_b64_e32 v[8:9], v[164:165]
	v_mov_b64_e32 v[10:11], v[166:167]
	v_mov_b64_e32 v[16:17], v[168:169]
	v_mov_b64_e32 v[18:19], v[170:171]
	v_mov_b64_e32 v[12:13], v[172:173]
	v_mov_b64_e32 v[14:15], v[174:175]
	v_add_u32_e32 v70, 0, v52
	v_add_u32_e32 v72, 0x20000, v70
	ds_read_b128 v[114:117], v72
	v_add_u32_e32 v72, 0x20010, v70
	ds_read_b128 v[118:121], v72
	v_add_u32_e32 v72, 0, v62
	v_add_u32_e32 v74, 0x10000, v72
	s_mov_b64 s[50:51], 0x100
	v_lshl_add_u64 v[88:89], v[88:89], 0, s[50:51]
	s_mov_b64 s[50:51], 0x200
	s_add_i32 s48, s48, -1
	v_lshl_add_u64 v[84:85], v[84:85], 0, s[50:51]
	s_mov_b64 s[50:51], 0x80
	v_add_u32_e32 v62, 0x100, v62
	v_add_u32_e32 v52, 0x200, v52
	s_cmp_eq_u32 s48, 0
	s_cbranch_scc1 .Lrtpf_skip_b
	v_lshl_add_u64 v[176:177], s[52:53], 0, v[88:89]
	global_load_dwordx4 v[128:131], v[176:177], off offset:-128
	v_lshl_add_u64 v[180:181], s[52:53], 0, v[84:85]
	s_mov_b32 s49, 0x169000
	v_add_co_u32_e32 v182, vcc, s49, v180
	s_mov_b64 s[50:51], 0x169000
	s_nop 0
	v_addc_co_u32_e32 v183, vcc, 0, v181, vcc
	v_lshl_add_u64 v[178:179], v[180:181], 0, s[50:51]
	global_load_dwordx4 v[132:135], v[182:183], off
	global_load_dwordx4 v[136:139], v[178:179], off offset:16
	global_load_dwordx4 v[140:143], v[176:177], off offset:-64
	s_mov_b64 s[50:51], 0x169080
	v_lshl_add_u64 v[178:179], v[180:181], 0, s[50:51]
	global_load_dwordx4 v[144:147], v[182:183], off offset:128
	global_load_dwordx4 v[148:151], v[178:179], off offset:16
	global_load_dwordx4 v[152:155], v[176:177], off
	s_mov_b64 s[50:51], 0x169100
	v_lshl_add_u64 v[178:179], v[180:181], 0, s[50:51]
	s_mov_b64 s[50:51], 0x169180
	v_lshl_add_u64 v[180:181], v[180:181], 0, s[50:51]
	global_load_dwordx4 v[156:159], v[182:183], off offset:256
	global_load_dwordx4 v[160:163], v[178:179], off offset:16
	global_load_dwordx4 v[164:167], v[176:177], off offset:64
	global_load_dwordx4 v[168:171], v[182:183], off offset:384
	global_load_dwordx4 v[172:175], v[180:181], off offset:16
	s_mov_b64 s[50:51], 0x80
.Lrtpf_skip_b:
	v_lshlrev_b32_e32 v90, 16, v44
	v_and_b32_e32 v91, 0xffff0000, v44
	v_pk_mul_f32 v[90:91], v[82:83], v[90:91]
	s_waitcnt lgkmcnt(1)
	v_pk_fma_f32 v[90:91], v[90:91], v[114:115], v[48:49]
	v_lshlrev_b32_e32 v114, 16, v45
	v_and_b32_e32 v115, 0xffff0000, v45
	v_pk_mul_f32 v[114:115], v[82:83], v[114:115]
	v_cvt_pk_bf16_f32 v44, v90, v91
	v_pk_fma_f32 v[114:115], v[114:115], v[116:117], v[50:51]
	v_lshlrev_b32_e32 v48, 16, v44
	v_cvt_pk_bf16_f32 v45, v114, v115
	v_and_b32_e32 v49, 0xffff0000, v44
	v_lshlrev_b32_e32 v50, 16, v45
	v_and_b32_e32 v51, 0xffff0000, v45
	v_pk_add_f32 v[48:49], v[90:91], v[48:49] neg_lo:[0,1] neg_hi:[0,1]
	v_pk_add_f32 v[50:51], v[114:115], v[50:51] neg_lo:[0,1] neg_hi:[0,1]
	v_cvt_pk_bf16_f32 v48, v48, v49
	v_cvt_pk_bf16_f32 v49, v50, v51
	v_lshlrev_b32_e32 v50, 16, v46
	v_and_b32_e32 v51, 0xffff0000, v46
	v_lshlrev_b32_e32 v116, 16, v47
	v_and_b32_e32 v117, 0xffff0000, v47
	v_pk_mul_f32 v[50:51], v[82:83], v[50:51]
	v_pk_mul_f32 v[116:117], v[82:83], v[116:117]
	s_waitcnt lgkmcnt(0)
	v_pk_fma_f32 v[110:111], v[50:51], v[118:119], v[110:111]
	v_pk_fma_f32 v[112:113], v[116:117], v[120:121], v[112:113]
	v_cvt_pk_bf16_f32 v46, v110, v111
	v_cvt_pk_bf16_f32 v47, v112, v113
	v_lshlrev_b32_e32 v50, 16, v46
	v_and_b32_e32 v51, 0xffff0000, v46
	v_lshlrev_b32_e32 v116, 16, v47
	v_and_b32_e32 v117, 0xffff0000, v47
	v_pk_add_f32 v[50:51], v[110:111], v[50:51] neg_lo:[0,1] neg_hi:[0,1]
	v_pk_add_f32 v[116:117], v[112:113], v[116:117] neg_lo:[0,1] neg_hi:[0,1]
	v_cvt_pk_bf16_f32 v50, v50, v51
	v_cvt_pk_bf16_f32 v51, v116, v117
	v_mov_b32_e32 v117, 0
	v_cvt_pk_fp8_f32 v117, v110, v111
	v_mov_b32_e32 v116, 0
	v_cvt_pk_fp8_f32 v116, v90, v91
	v_lshl_add_u64 v[90:91], s[52:53], 0, v[86:87]
	v_cvt_pk_fp8_f32 v117, v112, v113 op_sel:[0,0,1]
	ds_read_b128 v[110:113], v72
	v_cvt_pk_fp8_f32 v116, v114, v115 op_sel:[0,0,1]
	s_waitcnt lgkmcnt(0)
	v_mfma_f32_16x16x32_bf16 v[4:7], v[44:47], v[110:113], v[4:7]
	global_store_dwordx2 v[90:91], v[116:117], off offset:-64
	ds_read_b128 v[114:117], v74
	v_lshl_add_u64 v[86:87], v[86:87], 0, s[50:51]
	v_mfma_f32_16x16x32_bf16 v[4:7], v[48:51], v[110:113], v[4:7]
	ds_read_b128 v[110:113], v72 offset:32768
	v_add_u32_e32 v72, 0x18000, v72
	s_waitcnt lgkmcnt(0)
	v_mfma_f32_16x16x32_bf16 v[0:3], v[44:47], v[110:113], v[0:3]
	v_mfma_f32_16x16x32_bf16 v[4:7], v[44:47], v[114:117], v[4:7]
	ds_read_b128 v[114:117], v72
	v_mfma_f32_16x16x32_bf16 v[0:3], v[48:51], v[110:113], v[0:3]
	v_lshlrev_b32_e32 v110, 16, v32
	v_and_b32_e32 v111, 0xffff0000, v32
	v_add_u32_e32 v48, 0x20090, v70
	s_waitcnt lgkmcnt(0)
	v_mfma_f32_16x16x32_bf16 v[0:3], v[44:47], v[114:117], v[0:3]
	v_add_u32_e32 v44, 0x20080, v70
	ds_read_b128 v[44:47], v44
	ds_read_b128 v[48:51], v48
	v_pk_mul_f32 v[110:111], v[82:83], v[110:111]
	s_waitcnt lgkmcnt(1)
	v_pk_fma_f32 v[44:45], v[110:111], v[44:45], v[40:41]
	v_lshlrev_b32_e32 v110, 16, v33
	v_and_b32_e32 v111, 0xffff0000, v33
	v_pk_mul_f32 v[110:111], v[82:83], v[110:111]
	v_cvt_pk_bf16_f32 v32, v44, v45
	v_pk_fma_f32 v[46:47], v[110:111], v[46:47], v[42:43]
	v_lshlrev_b32_e32 v40, 16, v32
	v_cvt_pk_bf16_f32 v33, v46, v47
	v_and_b32_e32 v41, 0xffff0000, v32
	v_lshlrev_b32_e32 v42, 16, v33
	v_and_b32_e32 v43, 0xffff0000, v33
	v_pk_add_f32 v[40:41], v[44:45], v[40:41] neg_lo:[0,1] neg_hi:[0,1]
	v_pk_add_f32 v[42:43], v[46:47], v[42:43] neg_lo:[0,1] neg_hi:[0,1]
	v_cvt_pk_bf16_f32 v40, v40, v41
	v_cvt_pk_bf16_f32 v41, v42, v43
	v_lshlrev_b32_e32 v42, 16, v34
	v_and_b32_e32 v43, 0xffff0000, v34
	v_pk_mul_f32 v[42:43], v[82:83], v[42:43]
	s_waitcnt lgkmcnt(0)
	v_pk_fma_f32 v[36:37], v[42:43], v[48:49], v[36:37]
	v_lshlrev_b32_e32 v48, 16, v35
	v_and_b32_e32 v49, 0xffff0000, v35
	v_pk_mul_f32 v[48:49], v[82:83], v[48:49]
	v_cvt_pk_bf16_f32 v34, v36, v37
	v_pk_fma_f32 v[38:39], v[48:49], v[50:51], v[38:39]
	v_lshlrev_b32_e32 v42, 16, v34
	v_cvt_pk_bf16_f32 v35, v38, v39
	v_and_b32_e32 v43, 0xffff0000, v34
	v_lshlrev_b32_e32 v48, 16, v35
	v_and_b32_e32 v49, 0xffff0000, v35
	v_pk_add_f32 v[42:43], v[36:37], v[42:43] neg_lo:[0,1] neg_hi:[0,1]
	v_pk_add_f32 v[48:49], v[38:39], v[48:49] neg_lo:[0,1] neg_hi:[0,1]
	v_cvt_pk_bf16_f32 v42, v42, v43
	v_cvt_pk_bf16_f32 v43, v48, v49
	v_mov_b32_e32 v48, 0
	v_mov_b32_e32 v49, 0
	v_cvt_pk_fp8_f32 v48, v44, v45
	v_cvt_pk_fp8_f32 v49, v36, v37
	v_cvt_pk_fp8_f32 v48, v46, v47 op_sel:[0,0,1]
	v_cvt_pk_fp8_f32 v49, v38, v39 op_sel:[0,0,1]
	global_store_dwordx2 v[90:91], v[48:49], off offset:-32
	v_add_u32_e32 v48, 0, v64
	ds_read_b128 v[36:39], v48
	s_waitcnt lgkmcnt(0)
	v_mfma_f32_16x16x32_bf16 v[4:7], v[32:35], v[36:39], v[4:7]
	v_add_u32_e32 v44, 0x10000, v48
	ds_read_b128 v[44:47], v44
	v_add_u32_e32 v64, 0x100, v64
	v_mfma_f32_16x16x32_bf16 v[4:7], v[40:43], v[36:39], v[4:7]
	ds_read_b128 v[36:39], v48 offset:32768
	s_waitcnt lgkmcnt(0)
	v_mfma_f32_16x16x32_bf16 v[0:3], v[32:35], v[36:39], v[0:3]
	v_mfma_f32_16x16x32_bf16 v[4:7], v[32:35], v[44:47], v[4:7]
	v_add_u32_e32 v44, 0x18000, v48
	ds_read_b128 v[44:47], v44
	v_mfma_f32_16x16x32_bf16 v[0:3], v[40:43], v[36:39], v[0:3]
	v_lshlrev_b32_e32 v40, 16, v20
	v_and_b32_e32 v41, 0xffff0000, v20
	v_add_u32_e32 v36, 0x20110, v70
	s_waitcnt lgkmcnt(0)
	v_mfma_f32_16x16x32_bf16 v[0:3], v[32:35], v[44:47], v[0:3]
	v_add_u32_e32 v32, 0x20100, v70
	ds_read_b128 v[32:35], v32
	ds_read_b128 v[36:39], v36
	v_pk_mul_f32 v[40:41], v[82:83], v[40:41]
	s_waitcnt lgkmcnt(1)
	v_pk_fma_f32 v[32:33], v[40:41], v[32:33], v[28:29]
	v_lshlrev_b32_e32 v40, 16, v21
	v_and_b32_e32 v41, 0xffff0000, v21
	v_pk_mul_f32 v[40:41], v[82:83], v[40:41]
	v_cvt_pk_bf16_f32 v20, v32, v33
	v_pk_fma_f32 v[34:35], v[40:41], v[34:35], v[30:31]
	v_lshlrev_b32_e32 v28, 16, v20
	v_cvt_pk_bf16_f32 v21, v34, v35
	v_and_b32_e32 v29, 0xffff0000, v20
	v_lshlrev_b32_e32 v30, 16, v21
	v_and_b32_e32 v31, 0xffff0000, v21
	v_pk_add_f32 v[28:29], v[32:33], v[28:29] neg_lo:[0,1] neg_hi:[0,1]
	v_pk_add_f32 v[30:31], v[34:35], v[30:31] neg_lo:[0,1] neg_hi:[0,1]
	v_cvt_pk_bf16_f32 v28, v28, v29
	v_cvt_pk_bf16_f32 v29, v30, v31
	v_lshlrev_b32_e32 v30, 16, v22
	v_and_b32_e32 v31, 0xffff0000, v22
	v_pk_mul_f32 v[30:31], v[82:83], v[30:31]
	s_waitcnt lgkmcnt(0)
	v_pk_fma_f32 v[24:25], v[30:31], v[36:37], v[24:25]
	v_lshlrev_b32_e32 v36, 16, v23
	v_and_b32_e32 v37, 0xffff0000, v23
	v_pk_mul_f32 v[36:37], v[82:83], v[36:37]
	v_cvt_pk_bf16_f32 v22, v24, v25
	v_pk_fma_f32 v[26:27], v[36:37], v[38:39], v[26:27]
	v_lshlrev_b32_e32 v30, 16, v22
	v_cvt_pk_bf16_f32 v23, v26, v27
	v_and_b32_e32 v31, 0xffff0000, v22
	v_lshlrev_b32_e32 v36, 16, v23
	v_and_b32_e32 v37, 0xffff0000, v23
	v_pk_add_f32 v[30:31], v[24:25], v[30:31] neg_lo:[0,1] neg_hi:[0,1]
	v_pk_add_f32 v[36:37], v[26:27], v[36:37] neg_lo:[0,1] neg_hi:[0,1]
	v_cvt_pk_bf16_f32 v30, v30, v31
	v_cvt_pk_bf16_f32 v31, v36, v37
	v_mov_b32_e32 v36, 0
	v_mov_b32_e32 v37, 0
	v_cvt_pk_fp8_f32 v36, v32, v33
	v_cvt_pk_fp8_f32 v37, v24, v25
	v_cvt_pk_fp8_f32 v36, v34, v35 op_sel:[0,0,1]
	v_cvt_pk_fp8_f32 v37, v26, v27 op_sel:[0,0,1]
	global_store_dwordx2 v[90:91], v[36:37], off
	v_add_u32_e32 v36, 0, v66
	ds_read_b128 v[24:27], v36
	s_waitcnt lgkmcnt(0)
	v_mfma_f32_16x16x32_bf16 v[4:7], v[20:23], v[24:27], v[4:7]
	v_add_u32_e32 v32, 0x10000, v36
	ds_read_b128 v[32:35], v32
	v_add_u32_e32 v66, 0x100, v66
	v_mfma_f32_16x16x32_bf16 v[4:7], v[28:31], v[24:27], v[4:7]
	ds_read_b128 v[24:27], v36 offset:32768
	s_waitcnt lgkmcnt(0)
	v_mfma_f32_16x16x32_bf16 v[0:3], v[20:23], v[24:27], v[0:3]
	v_mfma_f32_16x16x32_bf16 v[4:7], v[20:23], v[32:35], v[4:7]
	v_add_u32_e32 v32, 0x18000, v36
	ds_read_b128 v[32:35], v32
	v_mfma_f32_16x16x32_bf16 v[0:3], v[28:31], v[24:27], v[0:3]
	v_lshlrev_b32_e32 v28, 16, v8
	v_and_b32_e32 v29, 0xffff0000, v8
	v_add_u32_e32 v24, 0x20190, v70
	s_waitcnt lgkmcnt(0)
	v_mfma_f32_16x16x32_bf16 v[0:3], v[20:23], v[32:35], v[0:3]
	v_add_u32_e32 v20, 0x20180, v70
	ds_read_b128 v[20:23], v20
	ds_read_b128 v[24:27], v24
	v_pk_mul_f32 v[28:29], v[82:83], v[28:29]
	s_waitcnt lgkmcnt(1)
	v_pk_fma_f32 v[20:21], v[28:29], v[20:21], v[16:17]
	v_lshlrev_b32_e32 v28, 16, v9
	v_and_b32_e32 v29, 0xffff0000, v9
	v_pk_mul_f32 v[28:29], v[82:83], v[28:29]
	v_cvt_pk_bf16_f32 v8, v20, v21
	v_pk_fma_f32 v[22:23], v[28:29], v[22:23], v[18:19]
	v_lshlrev_b32_e32 v16, 16, v8
	v_cvt_pk_bf16_f32 v9, v22, v23
	v_and_b32_e32 v17, 0xffff0000, v8
	v_lshlrev_b32_e32 v18, 16, v9
	v_and_b32_e32 v19, 0xffff0000, v9
	v_pk_add_f32 v[16:17], v[20:21], v[16:17] neg_lo:[0,1] neg_hi:[0,1]
	v_pk_add_f32 v[18:19], v[22:23], v[18:19] neg_lo:[0,1] neg_hi:[0,1]
	v_cvt_pk_bf16_f32 v16, v16, v17
	v_cvt_pk_bf16_f32 v17, v18, v19
	v_lshlrev_b32_e32 v18, 16, v10
	v_and_b32_e32 v19, 0xffff0000, v10
	v_pk_mul_f32 v[18:19], v[82:83], v[18:19]
	s_waitcnt lgkmcnt(0)
	v_pk_fma_f32 v[12:13], v[18:19], v[24:25], v[12:13]
	v_lshlrev_b32_e32 v24, 16, v11
	v_and_b32_e32 v25, 0xffff0000, v11
	v_pk_mul_f32 v[24:25], v[82:83], v[24:25]
	v_cvt_pk_bf16_f32 v10, v12, v13
	v_pk_fma_f32 v[14:15], v[24:25], v[26:27], v[14:15]
	v_lshlrev_b32_e32 v18, 16, v10
	v_cvt_pk_bf16_f32 v11, v14, v15
	v_and_b32_e32 v19, 0xffff0000, v10
	v_lshlrev_b32_e32 v24, 16, v11
	v_and_b32_e32 v25, 0xffff0000, v11
	v_pk_add_f32 v[18:19], v[12:13], v[18:19] neg_lo:[0,1] neg_hi:[0,1]
	v_pk_add_f32 v[24:25], v[14:15], v[24:25] neg_lo:[0,1] neg_hi:[0,1]
	v_cvt_pk_bf16_f32 v18, v18, v19
	v_cvt_pk_bf16_f32 v19, v24, v25
	v_mov_b32_e32 v24, 0
	v_mov_b32_e32 v25, 0
	v_cvt_pk_fp8_f32 v24, v20, v21
	v_cvt_pk_fp8_f32 v25, v12, v13
	v_cvt_pk_fp8_f32 v24, v22, v23 op_sel:[0,0,1]
	v_cvt_pk_fp8_f32 v25, v14, v15 op_sel:[0,0,1]
	global_store_dwordx2 v[90:91], v[24:25], off offset:32
	v_add_u32_e32 v24, 0, v68
	ds_read_b128 v[12:15], v24
	s_waitcnt lgkmcnt(0)
	v_mfma_f32_16x16x32_bf16 v[4:7], v[8:11], v[12:15], v[4:7]
	v_add_u32_e32 v20, 0x10000, v24
	ds_read_b128 v[20:23], v20
	v_add_u32_e32 v68, 0x100, v68
	v_mfma_f32_16x16x32_bf16 v[4:7], v[16:19], v[12:15], v[4:7]
	ds_read_b128 v[12:15], v24 offset:32768
	s_waitcnt lgkmcnt(0)
	v_mfma_f32_16x16x32_bf16 v[0:3], v[8:11], v[12:15], v[0:3]
	v_mfma_f32_16x16x32_bf16 v[4:7], v[8:11], v[20:23], v[4:7]
	v_add_u32_e32 v20, 0x18000, v24
	ds_read_b128 v[20:23], v20
	v_mfma_f32_16x16x32_bf16 v[0:3], v[16:19], v[12:15], v[0:3]
	s_waitcnt lgkmcnt(0)
	v_mfma_f32_16x16x32_bf16 v[0:3], v[8:11], v[20:23], v[0:3]
	s_cbranch_scc0 .LBB0_1663
	global_load_dword v8, v[60:61], off offset:128
	global_load_dword v9, v[60:61], off offset:192
	s_waitcnt vmcnt(1)
	v_add_f32_e32 v4, v4, v8
	s_waitcnt vmcnt(0)
	s_nop 1
	v_add_f32_e32 v0, v0, v9
	v_add_f32_e32 v5, v5, v8
	v_add_f32_e32 v6, v6, v8
	v_add_f32_e32 v7, v7, v8
	v_add_f32_e32 v1, v1, v9
	v_add_f32_e32 v2, v2, v9
	v_add_f32_e32 v3, v3, v9
	ds_write2_b32 v95, v4, v0 offset1:16
	ds_write2_b32 v95, v5, v1 offset0:32 offset1:48
	ds_write2_b32 v95, v6, v2 offset0:64 offset1:80
	ds_write2_b32 v95, v7, v3 offset0:96 offset1:112
	ds_read_b128 v[28:31], v107
	ds_read_b128 v[24:27], v107 offset:16
	ds_read_b128 v[20:23], v107 offset:32
	ds_read_b128 v[16:19], v107 offset:48
	ds_read_b128 v[12:15], v107 offset:64
	ds_read_b128 v[8:11], v107 offset:80
	ds_read_b128 v[4:7], v107 offset:96
	ds_read_b128 v[0:3], v107 offset:112
	s_waitcnt lgkmcnt(7)
	v_mov_b32_e32 v52, v28
	s_waitcnt lgkmcnt(3)
	v_mov_b32_e32 v32, v12
	s_and_saveexec_b64 s[48:49], s[6:7]
	s_cbranch_execz .LBB0_1670
	v_cmp_lt_i32_e32 vcc, 1, v94
	s_mov_b64 s[54:55], 0
	s_and_saveexec_b64 s[50:51], vcc
	s_xor_b64 s[56:57], exec, s[50:51]
	s_cbranch_execnz .LBB0_1737
	s_andn2_saveexec_b64 s[56:57], s[56:57]
	s_cbranch_execnz .LBB0_1740
